# attention phase: per-MFMA-group s_setprio flips deleted, one static priority raise for waves 4-7 for the whole phase (on top of the GEMM k-loop static raise)
# baseline (speedup 1.0000x reference)
.LBB0_895:
	v_lshl_add_u64 v[6:7], v[2:3], 2, s[6:7]
	global_load_dword v5, v[6:7], off
	v_add_u32_e32 v4, 0x200, v4
	v_cmp_lt_u32_e32 vcc, s2, v4
	v_add_u32_e32 v2, 4, v2
	s_or_b64 s[0:1], vcc, s[0:1]
	s_waitcnt vmcnt(0)
	v_mul_f32_e32 v5, 0x3fb8aa3b, v5
	ds_write_b32 v1, v5
	v_add_u32_e32 v1, 0x800, v1
	s_andn2_b64 exec, exec, s[0:1]
	s_cbranch_execnz .LBB0_895
	s_or_b64 exec, exec, s[0:1]
	v_readfirstlane_b32 s98, v0
	s_nop 3
	s_lshr_b32 s98, s98, 6
	s_cmp_ge_u32 s98, 4
	s_cbranch_scc0 .Lprio_att
	s_setprio 1
.Lprio_att:
	v_lshrrev_b32_e32 v5, 6, v0
	v_lshrrev_b32_e32 v6, 4, v166
	v_lshl_add_u32 v6, v5, 3, v6
	v_add_u32_e32 v7, 4, v6
	v_and_b32_e32 v8, 0xffffffe0, v6
	v_lshlrev_b32_e32 v1, 1, v6
	v_and_b32_e32 v1, 24, v1
	v_lshrrev_b32_e32 v2, 2, v6
	v_and_b32_e32 v2, 4, v2
	v_or3_b32 v8, v8, v1, v2
	v_and_b32_e32 v1, 3, v6
	v_or_b32_e32 v8, v8, v1
	v_xor_b32_e32 v9, v6, v166
	v_and_b32_e32 v9, 15, v9
	v_lshlrev_b32_e32 v9, 4, v9
	v_and_b32_e32 v10, 0xffffffe0, v7
	v_lshlrev_b32_e32 v1, 1, v7
	v_and_b32_e32 v1, 24, v1
	v_lshrrev_b32_e32 v2, 2, v7
	v_and_b32_e32 v2, 4, v2
	v_or3_b32 v10, v10, v1, v2
	v_and_b32_e32 v1, 3, v7
	v_or_b32_e32 v10, v10, v1
	v_xor_b32_e32 v11, v7, v166
	v_and_b32_e32 v11, 15, v11
	v_lshlrev_b32_e32 v11, 4, v11
	v_lshrrev_b32_e32 v16, 3, v166
	v_lshl_add_u32 v16, v5, 4, v16
	v_add_u32_e32 v17, 8, v16
	v_lshrrev_b32_e32 v18, 1, v16
	v_xor_b32_e32 v18, v18, v166
	v_and_b32_e32 v18, 7, v18
	v_lshlrev_b32_e32 v18, 4, v18
	v_lshrrev_b32_e32 v19, 1, v17
	v_xor_b32_e32 v19, v19, v166
	v_and_b32_e32 v19, 7, v19
	v_lshlrev_b32_e32 v19, 4, v19
	v_lshl_or_b32 v12, v8, 8, v9
	v_lshl_or_b32 v13, v10, 8, v11
	v_lshl_or_b32 v14, v16, 10, v18
	v_lshl_or_b32 v15, v17, 10, v19
	v_lshl_or_b32 v20, v8, 12, v9
	v_lshl_or_b32 v21, v10, 12, v11
	v_lshl_or_b32 v22, v16, 15, v18
	v_lshl_or_b32 v23, v17, 15, v19
	v_lshlrev_b32_e32 v1, 4, v0
	v_add_u32_e32 v1, 0x24000, v1
	ds_write_b128 v1, v[12:15]
	ds_write_b128 v1, v[20:23] offset:8192
	s_cmpk_gt_i32 s90, 0x3ff
	s_waitcnt lgkmcnt(0)
	s_barrier
	s_cbranch_scc1 .LBB0_1273
	v_writelane_b32 v255, s40, 11
	v_cmp_ne_u32_e64 s[10:11], 0, v166
	v_and_b32_e32 v1, 15, v0
	v_writelane_b32 v255, s41, 12
	v_writelane_b32 v255, s62, 13
	v_bfe_u32 v230, v0, 2, 2
	v_lshrrev_b32_e32 v4, 4, v166
	v_writelane_b32 v255, s63, 14
	v_writelane_b32 v255, s10, 15
	v_bitop3_b32 v5, v4, v0, 15 bitop3:0x78
	v_lshlrev_b32_e32 v209, 4, v5
	v_writelane_b32 v255, s11, 16
	v_cmp_eq_u32_e64 s[10:11], 0, v166
	v_bitop3_b32 v5, v4, v1, 4 bitop3:0x36
	v_lshlrev_b32_e32 v210, 4, v5
	v_writelane_b32 v255, s10, 17
	v_bitop3_b32 v5, v4, v1, 8 bitop3:0x36
	s_lshl_b32 s0, s92, 12
	v_writelane_b32 v255, s11, 18
	v_cmp_gt_u32_e64 s[10:11], 4, v1
	v_and_b32_e32 v2, 48, v166
	v_mov_b32_e32 v3, 0
	v_writelane_b32 v255, s10, 19
	s_lshl_b32 s8, s92, 11
	v_lshlrev_b32_e32 v211, 4, v5
	v_writelane_b32 v255, s11, 20
	v_cmp_eq_u32_e64 s[10:11], 1, v230
	v_bitop3_b32 v5, v4, v1, 12 bitop3:0x36
	v_lshl_add_u64 v[252:253], s[62:63], 0, v[2:3]
	v_writelane_b32 v255, s10, 21
	s_add_i32 s1, s0, 0
	s_sub_i32 s6, 0, s8
	v_writelane_b32 v255, s11, 22
	v_cmp_eq_u32_e64 s[10:11], 2, v230
	v_lshlrev_b32_e32 v2, 8, v1
	v_lshlrev_b32_e32 v212, 4, v5
	v_writelane_b32 v255, s10, 23
	s_mov_b32 s7, 0xa000
	v_add_u32_e32 v218, 0, v2
	v_writelane_b32 v255, s11, 24
	v_cmp_eq_u32_e64 s[10:11], 3, v230
	v_or3_b32 v232, v2, v212, s7
	v_or3_b32 v233, v2, v211, s7
	v_writelane_b32 v255, s10, 25
	v_or3_b32 v234, v2, v210, s7
	v_or3_b32 v235, v2, v209, s7
	v_writelane_b32 v255, s11, 26
	v_writelane_b32 v255, s8, 27
	v_lshl_or_b32 v2, v230, 9, s0
	s_add_i32 s0, s1, s6
	v_writelane_b32 v255, s0, 28
	s_add_i32 s0, 0, 0x12000
	v_writelane_b32 v255, s0, 29
	s_add_i32 s0, 0, 0x16000
	v_writelane_b32 v255, s0, 30
	v_add_u32_e32 v5, 48, v0
	v_bfe_u32 v6, v0, 1, 3
	v_writelane_b32 v255, s96, 31
	s_lshl_b32 s73, s92, 3
	s_lshl_b32 s81, s92, 4
	v_and_b32_e32 v213, 63, v5
	v_lshlrev_b32_e32 v5, 7, v1
	v_xor_b32_e32 v7, v6, v4
	v_bitop3_b32 v6, v4, v6, 4 bitop3:0x36
	v_mul_i32_i24_e32 v1, -8, v4
	v_writelane_b32 v255, s97, 32
	v_and_b32_e32 v179, 3, v0
	v_lshlrev_b32_e32 v208, 3, v4
	s_or_b32 s65, s73, 4
	s_or_b32 s78, s81, 8
	v_lshlrev_b32_e32 v216, 2, v4
	v_lshl_add_u32 v215, v166, 2, s1
	v_lshlrev_b32_e32 v4, 7, v4
	v_lshl_or_b32 v220, v6, 4, v5
	v_lshl_or_b32 v225, v7, 4, v5
	v_or_b32_e32 v239, v1, v230
	v_mbcnt_lo_u32_b32 v1, -1, 0
	v_writelane_b32 v254, s60, 7
	v_writelane_b32 v255, s94, 33
	s_lshl_b32 s85, s65, 8
	s_lshl_b32 s40, s78, 7
	v_cmp_gt_u32_e64 s[2:3], 16, v166
	v_cmp_eq_u32_e64 s[4:5], 0, v179
	v_or_b32_e32 v214, 64, v166
	v_add_u32_e32 v217, 0x2000, v215
	v_or_b32_e32 v247, 0xffffffc0, v166
	v_sub_u32_e32 v219, v230, v4
	s_add_i32 s33, s8, 0
	v_or_b32_e32 v221, 0x10000, v220
	v_or_b32_e32 v222, 0x10800, v220
	v_or_b32_e32 v223, 0x11000, v220
	v_or_b32_e32 v224, 0x11800, v220
	v_or_b32_e32 v226, 0x10000, v225
	v_or_b32_e32 v227, 0x10800, v225
	v_or_b32_e32 v228, 0x11000, v225
	v_or_b32_e32 v229, 0x11800, v225
	v_or_b32_e32 v231, 0x270, v4
	s_add_i32 s64, s8, 0x1e400
	s_add_i32 s80, s8, 0x1a400
	s_add_i32 s79, s8, 0x1e000
	s_add_i32 s58, s8, 0x1a000
	v_add_u32_e32 v236, 0, v208
	v_add_u32_e32 v237, 0x2000, v2
	v_sub_u32_e32 v238, v230, v208
	s_movk_i32 s59, 0xff84
	v_mov_b32_e32 v173, 0x41000000
	s_movk_i32 s62, 0x200
	v_lshlrev_b32_e32 v174, 2, v216
	v_mov_b32_e32 v176, 0xf149f2ca
	v_mov_b32_e32 v240, 0x9e
	v_mov_b32_e32 v241, 0xff61b1e6
	v_mbcnt_hi_u32_b32 v242, -1, v1
	v_mov_b32_e32 v243, 0x7f
	s_mov_b32 s63, s90
	v_writelane_b32 v254, s61, 8
	v_writelane_b32 v255, s95, 34
	s_branch .LBB0_899

.LBB0_940:
	s_cmp_gt_i32 s52, s9
	s_cbranch_scc1 .LBB0_924
	s_mul_hi_u32 s6, s61, 0xaaaaaaab
	s_lshr_b32 s6, s6, 1
	s_mul_i32 s6, s6, 0x18000
	v_subrev_u32_e32 v46, s6, v212
	v_subrev_u32_e32 v47, s6, v211
	v_subrev_u32_e32 v48, s6, v210
	v_subrev_u32_e32 v49, s6, v209
	s_add_i32 s30, s52, 63
	v_add_u32_e32 v50, s60, v218
	s_cmp_gt_i32 s52, s8
	v_add_u32_e32 v2, s52, v208
	v_add_u32_e32 v79, v50, v49
	v_add_u32_e32 v78, v50, v48
	v_add_u32_e32 v75, v50, v47
	v_add_u32_e32 v74, v50, v46
	s_cbranch_scc1 .LBB0_945
	ds_read_b128 v[38:41], v79 offset:40960
	ds_read_b128 v[42:45], v79 offset:45056
	ds_read_b128 v[46:49], v78 offset:40960
	ds_read_b128 v[50:53], v78 offset:45056
	ds_read_b128 v[54:57], v75 offset:40960
	ds_read_b128 v[62:65], v75 offset:45056
	ds_read_b128 v[58:61], v74 offset:40960
	ds_read_b128 v[66:69], v74 offset:45056
	s_waitcnt lgkmcnt(0)
	v_mfma_f32_16x16x32_f16 v[38:41], v[38:41], v[6:9], 0
	v_mfma_f32_16x16x32_f16 v[38:41], v[46:49], v[10:13], v[38:41]
	v_mfma_f32_16x16x32_f16 v[38:41], v[54:57], v[14:17], v[38:41]
	v_mfma_f32_16x16x32_f16 v[58:61], v[58:61], v[18:21], v[38:41]
	v_mfma_f32_16x16x32_f16 v[38:41], v[42:45], v[6:9], 0
	v_mfma_f32_16x16x32_f16 v[38:41], v[50:53], v[10:13], v[38:41]
	v_mfma_f32_16x16x32_f16 v[38:41], v[62:65], v[14:17], v[38:41]
	v_mfma_f32_16x16x32_f16 v[54:57], v[66:69], v[18:21], v[38:41]
	s_nop 5
	ds_read_b128 v[38:41], v79 offset:49152
	ds_read_b128 v[42:45], v79 offset:53248
	ds_read_b128 v[46:49], v78 offset:49152
	ds_read_b128 v[62:65], v78 offset:53248
	ds_read_b128 v[50:53], v75 offset:49152
	ds_read_b128 v[66:69], v75 offset:53248
	ds_read_b128 v[80:83], v74 offset:49152
	ds_read_b128 v[84:87], v74 offset:53248
	s_waitcnt lgkmcnt(0)
	v_mfma_f32_16x16x32_f16 v[38:41], v[38:41], v[6:9], 0
	v_mfma_f32_16x16x32_f16 v[38:41], v[46:49], v[10:13], v[38:41]
	v_mfma_f32_16x16x32_f16 v[38:41], v[50:53], v[14:17], v[38:41]
	v_mfma_f32_16x16x32_f16 v[50:53], v[80:83], v[18:21], v[38:41]
	v_mfma_f32_16x16x32_f16 v[38:41], v[42:45], v[6:9], 0
	v_mfma_f32_16x16x32_f16 v[38:41], v[62:65], v[10:13], v[38:41]
	v_mfma_f32_16x16x32_f16 v[38:41], v[66:69], v[14:17], v[38:41]
	v_mfma_f32_16x16x32_f16 v[46:49], v[84:87], v[18:21], v[38:41]
	s_cmp_le_i32 s30, s13
	s_cselect_b64 s[6:7], -1, 0
	s_cmpk_gt_i32 s47, 0x9d
	s_cselect_b64 s[34:35], -1, 0
	s_and_b64 s[34:35], s[6:7], s[34:35]
	s_mov_b64 s[6:7], -1
	s_and_b64 vcc, exec, s[34:35]
	s_cbranch_vccnz .LBB0_948
	v_add_u32_e32 v38, s47, v219
	v_add_u32_e32 v39, 0x3f0, v38
	v_add_u32_e32 v40, 0x3e0, v38
	v_add_u32_e32 v42, 0x3d0, v38
	v_add_u32_e32 v44, 0x3c0, v38
	v_add_u32_e32 v62, 0x3b0, v38
	v_add_u32_e32 v64, 0x3a0, v38
	v_add_u32_e32 v66, 0x390, v38
	v_add_u32_e32 v68, 0x380, v38
	v_med3_i32 v39, v39, 31, v240
	v_med3_i32 v40, v40, 31, v240
	v_med3_i32 v42, v42, 31, v240
	v_med3_i32 v44, v44, 31, v240
	v_med3_i32 v62, v62, 31, v240
	v_med3_i32 v64, v64, 31, v240
	v_med3_i32 v66, v66, 31, v240
	v_med3_i32 v68, v68, 31, v240
	v_lshlrev_b32_e32 v39, 2, v39
	v_lshlrev_b32_e32 v40, 2, v40
	v_lshlrev_b32_e32 v42, 2, v42
	v_lshlrev_b32_e32 v44, 2, v44
	v_lshlrev_b32_e32 v62, 2, v62
	v_lshlrev_b32_e32 v64, 2, v64
	v_lshlrev_b32_e32 v66, 2, v66
	v_lshlrev_b32_e32 v68, 2, v68
	v_add3_u32 v39, v244, v39, s59
	v_add3_u32 v40, v244, v40, s59
	v_add3_u32 v42, v244, v42, s59
	v_add3_u32 v44, v244, v44, s59
	v_add3_u32 v62, v244, v62, s59
	v_add3_u32 v64, v244, v64, s59
	v_add3_u32 v66, v244, v66, s59
	v_add3_u32 v68, v244, v68, s59
	ds_read_b32 v39, v39
	ds_read_b32 v40, v40
	ds_read_b32 v42, v42
	ds_read_b32 v44, v44
	ds_read_b32 v62, v62
	ds_read_b32 v64, v64
	ds_read_b32 v66, v66
	ds_read_b32 v72, v68
	v_add_u32_e32 v68, 0x1f0, v38
	v_add_u32_e32 v85, 0x1b0, v38
	v_add_u32_e32 v86, 0x1a0, v38
	v_add_u32_e32 v87, 0x190, v38
	v_med3_i32 v68, v68, 31, v240
	v_add_u32_e32 v69, 0x1e0, v38
	v_add_u32_e32 v80, 0x1d0, v38
	v_add_u32_e32 v81, 0x1c0, v38
	v_med3_i32 v85, v85, 31, v240
	v_med3_i32 v86, v86, 31, v240
	v_med3_i32 v87, v87, 31, v240
	v_add_u32_e32 v38, 0x180, v38
	v_lshlrev_b32_e32 v68, 2, v68
	v_med3_i32 v69, v69, 31, v240
	v_med3_i32 v80, v80, 31, v240
	v_med3_i32 v81, v81, 31, v240
	v_lshlrev_b32_e32 v85, 2, v85
	v_lshlrev_b32_e32 v86, 2, v86
	v_lshlrev_b32_e32 v87, 2, v87
	v_med3_i32 v38, v38, 31, v240
	v_add3_u32 v68, v244, v68, s59
	v_lshlrev_b32_e32 v69, 2, v69
	v_lshlrev_b32_e32 v80, 2, v80
	v_lshlrev_b32_e32 v81, 2, v81
	v_add3_u32 v85, v244, v85, s59
	v_add3_u32 v86, v244, v86, s59
	v_add3_u32 v87, v244, v87, s59
	v_lshlrev_b32_e32 v38, 2, v38
	v_add3_u32 v69, v244, v69, s59
	v_add3_u32 v80, v244, v80, s59
	v_add3_u32 v81, v244, v81, s59
	v_add3_u32 v38, v244, v38, s59
	ds_read_b32 v88, v68
	ds_read_b32 v89, v69
	ds_read_b32 v90, v80
	ds_read_b32 v91, v81
	ds_read_b32 v85, v85
	ds_read_b32 v86, v86
	ds_read_b32 v87, v87
	ds_read_b32 v92, v38
	v_add_u32_e32 v41, 2, v2
	v_add_u32_e32 v45, 4, v2
	v_add_u32_e32 v63, 5, v2
	v_add_u32_e32 v65, 6, v2
	v_add_u32_e32 v67, 7, v2
	v_add_u32_e32 v43, 3, v2
	v_add_u32_e32 v73, 32, v2
	v_add_u32_e32 v82, 33, v2
	v_add_u32_e32 v83, 34, v2
	v_add_u32_e32 v84, 35, v2
	v_add_u32_e32 v93, 36, v2
	v_add_u32_e32 v94, 37, v2
	v_add_u32_e32 v95, 38, v2
	v_add_u32_e32 v96, 39, v2
	s_waitcnt lgkmcnt(0)
	v_fmac_f32_e32 v39, 0x3e0293ee, v58
	v_cmp_le_i32_e32 vcc, v2, v76
	v_fmac_f32_e32 v40, 0x3e0293ee, v59
	v_fmac_f32_e32 v42, 0x3e0293ee, v60
	v_cndmask_b32_e32 v38, v241, v39, vcc
	v_cmp_lt_i32_e32 vcc, v2, v76
	v_fmac_f32_e32 v44, 0x3e0293ee, v61
	v_fmac_f32_e32 v62, 0x3e0293ee, v54
	v_cndmask_b32_e32 v39, v241, v40, vcc
	v_cmp_le_i32_e32 vcc, v41, v76
	v_fmac_f32_e32 v64, 0x3e0293ee, v55
	v_fmac_f32_e32 v66, 0x3e0293ee, v56
	v_cndmask_b32_e32 v41, v241, v42, vcc
	v_cmp_le_i32_e32 vcc, v43, v76
	v_fmac_f32_e32 v72, 0x3e0293ee, v57
	v_fmac_f32_e32 v88, 0x3e0293ee, v50
	v_cndmask_b32_e32 v69, v241, v44, vcc
	v_cmp_le_i32_e32 vcc, v45, v76
	v_fmac_f32_e32 v89, 0x3e0293ee, v51
	v_fmac_f32_e32 v90, 0x3e0293ee, v52
	v_cndmask_b32_e32 v40, v241, v62, vcc
	v_cmp_le_i32_e32 vcc, v63, v76
	v_max_f32_e32 v42, v38, v39
	v_fmac_f32_e32 v91, 0x3e0293ee, v53
	v_cndmask_b32_e32 v68, v241, v64, vcc
	v_cmp_le_i32_e32 vcc, v65, v76
	v_max3_f32 v42, v42, v41, v69
	v_fmac_f32_e32 v85, 0x3e0293ee, v46
	v_cndmask_b32_e32 v80, v241, v66, vcc
	v_cmp_le_i32_e32 vcc, v67, v76
	v_max3_f32 v42, v42, v40, v68
	v_fmac_f32_e32 v86, 0x3e0293ee, v47
	v_cndmask_b32_e32 v81, v241, v72, vcc
	v_cmp_le_i32_e32 vcc, v73, v76
	v_max3_f32 v42, v42, v80, v81
	v_fmac_f32_e32 v87, 0x3e0293ee, v48
	v_cndmask_b32_e32 v44, v241, v88, vcc
	v_cmp_le_i32_e32 vcc, v82, v76
	v_fmac_f32_e32 v92, 0x3e0293ee, v49
	v_add_f32_e32 v43, 0x41000000, v4
	v_cndmask_b32_e32 v45, v241, v89, vcc
	v_cmp_le_i32_e32 vcc, v83, v76
	v_max3_f32 v42, v42, v44, v45
	s_nop 0
	v_cndmask_b32_e32 v63, v241, v90, vcc
	v_cmp_le_i32_e32 vcc, v84, v76
	s_nop 1
	v_cndmask_b32_e32 v65, v241, v91, vcc
	v_cmp_le_i32_e32 vcc, v93, v76
	v_max3_f32 v42, v42, v63, v65
	s_nop 0
	v_cndmask_b32_e32 v62, v241, v85, vcc
	v_cmp_le_i32_e32 vcc, v94, v76
	s_nop 1
	v_cndmask_b32_e32 v64, v241, v86, vcc
	v_cmp_le_i32_e32 vcc, v95, v76
	v_max3_f32 v42, v42, v62, v64
	s_nop 0
	v_cndmask_b32_e32 v66, v241, v87, vcc
	v_cmp_le_i32_e32 vcc, v96, v76
	s_nop 1
	v_cndmask_b32_e32 v67, v241, v92, vcc
	v_max3_f32 v42, v42, v66, v67
	v_cmp_gt_f32_e32 vcc, v42, v43
	s_cbranch_vccz .LBB0_946
	v_and_b32_e32 v72, 64, v242
	v_xor_b32_e32 v43, 16, v242
	v_add_u32_e32 v72, 64, v72
	v_cmp_lt_i32_e32 vcc, v43, v72
	v_xor_b32_e32 v73, 32, v242
	s_nop 0
	v_cndmask_b32_e32 v43, v242, v43, vcc
	v_lshlrev_b32_e32 v43, 2, v43
	ds_bpermute_b32 v43, v43, v42
	v_max_f32_e32 v42, v42, v42
	v_cmp_lt_i32_e32 vcc, v73, v72
	s_waitcnt lgkmcnt(0)
	v_max_f32_e32 v43, v43, v43
	v_max_f32_e32 v42, v42, v43
	v_cndmask_b32_e32 v43, v242, v73, vcc
	v_lshlrev_b32_e32 v43, 2, v43
	ds_bpermute_b32 v43, v43, v42
	s_waitcnt lgkmcnt(0)
	v_max3_f32 v42, v4, v42, v43
	v_sub_f32_e32 v43, v4, v42
	v_exp_f32_e32 v82, v43
	v_mov_b32_e32 v43, v5
	v_mov_b64_e32 v[72:73], v[42:43]
	s_branch .LBB0_947

.LBB0_954:
	ds_read_b128 v[46:49], v79 offset:40960
	ds_read_b128 v[50:53], v79 offset:45056
	ds_read_b128 v[54:57], v78 offset:40960
	ds_read_b128 v[58:61], v78 offset:45056
	ds_read_b128 v[62:65], v75 offset:40960
	ds_read_b128 v[80:83], v75 offset:45056
	ds_read_b128 v[66:69], v74 offset:40960
	ds_read_b128 v[84:87], v74 offset:45056
	s_waitcnt lgkmcnt(0)
	v_mfma_f32_16x16x32_f16 v[46:49], v[46:49], v[22:25], 0
	v_mfma_f32_16x16x32_f16 v[46:49], v[54:57], v[26:29], v[46:49]
	v_mfma_f32_16x16x32_f16 v[46:49], v[62:65], v[30:33], v[46:49]
	v_mfma_f32_16x16x32_f16 v[66:69], v[66:69], v[34:37], v[46:49]
	v_mfma_f32_16x16x32_f16 v[46:49], v[50:53], v[22:25], 0
	v_mfma_f32_16x16x32_f16 v[46:49], v[58:61], v[26:29], v[46:49]
	v_mfma_f32_16x16x32_f16 v[46:49], v[80:83], v[30:33], v[46:49]
	v_mfma_f32_16x16x32_f16 v[62:65], v[84:87], v[34:37], v[46:49]
	s_nop 5
	ds_read_b128 v[46:49], v79 offset:49152
	ds_read_b128 v[50:53], v79 offset:53248
	ds_read_b128 v[54:57], v78 offset:49152
	ds_read_b128 v[78:81], v78 offset:53248
	ds_read_b128 v[58:61], v75 offset:49152
	ds_read_b128 v[82:85], v75 offset:53248
	ds_read_b128 v[86:89], v74 offset:49152
	ds_read_b128 v[90:93], v74 offset:53248
	s_waitcnt lgkmcnt(0)
	v_mfma_f32_16x16x32_f16 v[46:49], v[46:49], v[22:25], 0
	v_mfma_f32_16x16x32_f16 v[46:49], v[54:57], v[26:29], v[46:49]
	v_mfma_f32_16x16x32_f16 v[46:49], v[58:61], v[30:33], v[46:49]
	v_mfma_f32_16x16x32_f16 v[58:61], v[86:89], v[34:37], v[46:49]
	v_mfma_f32_16x16x32_f16 v[46:49], v[50:53], v[22:25], 0
	v_mfma_f32_16x16x32_f16 v[46:49], v[78:81], v[26:29], v[46:49]
	v_mfma_f32_16x16x32_f16 v[46:49], v[82:85], v[30:33], v[46:49]
	v_mfma_f32_16x16x32_f16 v[54:57], v[90:93], v[34:37], v[46:49]
	s_cmp_le_i32 s30, s46
	s_cselect_b64 s[6:7], -1, 0
	s_add_i32 s30, s47, 4
	s_cmpk_gt_i32 s30, 0x9d
	s_cselect_b64 s[30:31], -1, 0
	s_and_b64 s[30:31], s[6:7], s[30:31]
	s_mov_b64 s[6:7], -1
	s_and_b64 vcc, exec, s[30:31]
	s_cbranch_vccnz .LBB0_959
	v_add_u32_e32 v4, s47, v219
	v_add_u32_e32 v5, 0x3f4, v4
	v_add_u32_e32 v46, 0x3e4, v4
	v_add_u32_e32 v47, 0x3d4, v4
	v_add_u32_e32 v48, 0x3c4, v4
	v_add_u32_e32 v52, 0x3b4, v4
	v_add_u32_e32 v74, 0x3a4, v4
	v_add_u32_e32 v78, 0x394, v4
	v_add_u32_e32 v80, 0x384, v4
	v_med3_i32 v5, v5, 31, v240
	v_med3_i32 v46, v46, 31, v240
	v_med3_i32 v47, v47, 31, v240
	v_med3_i32 v48, v48, 31, v240
	v_med3_i32 v52, v52, 31, v240
	v_med3_i32 v74, v74, 31, v240
	v_med3_i32 v78, v78, 31, v240
	v_med3_i32 v80, v80, 31, v240
	v_lshlrev_b32_e32 v5, 2, v5
	v_lshlrev_b32_e32 v46, 2, v46
	v_lshlrev_b32_e32 v47, 2, v47
	v_lshlrev_b32_e32 v48, 2, v48
	v_lshlrev_b32_e32 v52, 2, v52
	v_lshlrev_b32_e32 v74, 2, v74
	v_lshlrev_b32_e32 v78, 2, v78
	v_lshlrev_b32_e32 v80, 2, v80
	v_add3_u32 v5, v244, v5, s59
	v_add3_u32 v46, v244, v46, s59
	v_add3_u32 v47, v244, v47, s59
	v_add3_u32 v48, v244, v48, s59
	v_add3_u32 v52, v244, v52, s59
	v_add3_u32 v74, v244, v74, s59
	v_add3_u32 v78, v244, v78, s59
	v_add3_u32 v80, v244, v80, s59
	ds_read_b32 v5, v5
	ds_read_b32 v46, v46
	ds_read_b32 v81, v47
	ds_read_b32 v82, v48
	ds_read_b32 v52, v52
	ds_read_b32 v74, v74
	ds_read_b32 v78, v78
	ds_read_b32 v80, v80
	v_add_u32_e32 v47, 0x1f4, v4
	v_add_u32_e32 v48, 0x1e4, v4
	v_add_u32_e32 v83, 0x1d4, v4
	v_add_u32_e32 v84, 0x1c4, v4
	v_add_u32_e32 v85, 0x1b4, v4
	v_add_u32_e32 v90, 0x1a4, v4
	v_add_u32_e32 v91, 0x194, v4
	v_add_u32_e32 v4, 0x184, v4
	v_med3_i32 v47, v47, 31, v240
	v_med3_i32 v90, v90, 31, v240
	v_med3_i32 v91, v91, 31, v240
	v_med3_i32 v4, v4, 31, v240
	v_lshlrev_b32_e32 v47, 2, v47
	v_med3_i32 v48, v48, 31, v240
	v_med3_i32 v83, v83, 31, v240
	v_med3_i32 v84, v84, 31, v240
	v_med3_i32 v85, v85, 31, v240
	v_lshlrev_b32_e32 v90, 2, v90
	v_lshlrev_b32_e32 v91, 2, v91
	v_lshlrev_b32_e32 v4, 2, v4
	v_add3_u32 v47, v244, v47, s59
	v_lshlrev_b32_e32 v48, 2, v48
	v_lshlrev_b32_e32 v83, 2, v83
	v_lshlrev_b32_e32 v84, 2, v84
	v_lshlrev_b32_e32 v85, 2, v85
	v_add3_u32 v90, v244, v90, s59
	v_add3_u32 v91, v244, v91, s59
	v_add3_u32 v4, v244, v4, s59
	v_add3_u32 v48, v244, v48, s59
	v_add3_u32 v83, v244, v83, s59
	v_add3_u32 v84, v244, v84, s59
	v_add3_u32 v85, v244, v85, s59
	ds_read_b32 v92, v47
	ds_read_b32 v93, v48
	ds_read_b32 v94, v83
	ds_read_b32 v95, v84
	ds_read_b32 v96, v85
	ds_read_b32 v90, v90
	ds_read_b32 v91, v91
	ds_read_b32 v4, v4
	v_add_u32_e32 v49, 2, v2
	v_add_u32_e32 v53, 5, v2
	v_add_u32_e32 v75, 6, v2
	v_add_u32_e32 v79, 7, v2
	v_add_u32_e32 v50, 3, v2
	v_add_u32_e32 v51, 4, v2
	v_add_u32_e32 v86, 32, v2
	v_add_u32_e32 v87, 33, v2
	v_add_u32_e32 v88, 34, v2
	v_add_u32_e32 v89, 35, v2
	v_add_u32_e32 v97, 36, v2
	v_add_u32_e32 v98, 37, v2
	v_add_u32_e32 v99, 38, v2
	v_add_u32_e32 v100, 39, v2
	s_waitcnt lgkmcnt(0)
	v_fmac_f32_e32 v5, 0x3e0293ee, v66
	v_cmp_le_i32_e32 vcc, v2, v77
	v_fmac_f32_e32 v46, 0x3e0293ee, v67
	v_fmac_f32_e32 v81, 0x3e0293ee, v68
	v_cndmask_b32_e32 v47, v241, v5, vcc
	v_cmp_lt_i32_e32 vcc, v2, v77
	v_fmac_f32_e32 v82, 0x3e0293ee, v69
	v_fmac_f32_e32 v52, 0x3e0293ee, v62
	v_cndmask_b32_e32 v48, v241, v46, vcc
	v_cmp_le_i32_e32 vcc, v49, v77
	v_fmac_f32_e32 v74, 0x3e0293ee, v63
	v_fmac_f32_e32 v78, 0x3e0293ee, v64
	v_cndmask_b32_e32 v81, v241, v81, vcc
	v_cmp_le_i32_e32 vcc, v50, v77
	v_fmac_f32_e32 v80, 0x3e0293ee, v65
	v_fmac_f32_e32 v92, 0x3e0293ee, v58
	v_cndmask_b32_e32 v83, v241, v82, vcc
	v_cmp_le_i32_e32 vcc, v51, v77
	v_fmac_f32_e32 v93, 0x3e0293ee, v59
	v_fmac_f32_e32 v94, 0x3e0293ee, v60
	v_cndmask_b32_e32 v49, v241, v52, vcc
	v_cmp_le_i32_e32 vcc, v53, v77
	v_fmac_f32_e32 v95, 0x3e0293ee, v61
	v_fmac_f32_e32 v96, 0x3e0293ee, v54
	v_cndmask_b32_e32 v82, v241, v74, vcc
	v_cmp_le_i32_e32 vcc, v75, v77
	v_fmac_f32_e32 v90, 0x3e0293ee, v55
	v_fmac_f32_e32 v91, 0x3e0293ee, v56
	v_cndmask_b32_e32 v84, v241, v78, vcc
	v_cmp_le_i32_e32 vcc, v79, v77
	v_fmac_f32_e32 v4, 0x3e0293ee, v57
	v_add_f32_e32 v5, 0x41000000, v73
	v_cndmask_b32_e32 v85, v241, v80, vcc
	v_cmp_le_i32_e32 vcc, v86, v77
	s_nop 1
	v_cndmask_b32_e32 v2, v241, v92, vcc
	v_cmp_le_i32_e32 vcc, v87, v77
	s_nop 1
	v_cndmask_b32_e32 v46, v241, v93, vcc
	v_cmp_le_i32_e32 vcc, v88, v77
	s_nop 1
	v_cndmask_b32_e32 v75, v241, v94, vcc
	v_cmp_le_i32_e32 vcc, v89, v77
	s_nop 1
	v_cndmask_b32_e32 v52, v241, v95, vcc
	v_cmp_le_i32_e32 vcc, v97, v77
	s_nop 1
	v_cndmask_b32_e32 v74, v241, v96, vcc
	v_cmp_le_i32_e32 vcc, v98, v77
	s_nop 1
	v_cndmask_b32_e32 v79, v241, v90, vcc
	v_cmp_le_i32_e32 vcc, v99, v77
	s_nop 1
	v_cndmask_b32_e32 v80, v241, v91, vcc
	v_cmp_le_i32_e32 vcc, v100, v77
	s_nop 1
	v_cndmask_b32_e32 v53, v241, v4, vcc
	v_max_f32_e32 v4, v47, v48
	v_max3_f32 v4, v4, v81, v83
	v_max3_f32 v4, v4, v49, v82
	v_max3_f32 v4, v4, v84, v85
	v_max3_f32 v4, v4, v2, v46
	v_max3_f32 v4, v4, v75, v52
	v_max3_f32 v4, v4, v74, v79
	v_max3_f32 v4, v4, v80, v53
	v_cmp_gt_f32_e32 vcc, v4, v5
	s_cbranch_vccz .LBB0_957
	v_and_b32_e32 v50, 64, v242
	v_xor_b32_e32 v5, 16, v242
	v_add_u32_e32 v50, 64, v50
	v_cmp_lt_i32_e32 vcc, v5, v50
	v_xor_b32_e32 v51, 32, v242
	s_nop 0
	v_cndmask_b32_e32 v5, v242, v5, vcc
	v_lshlrev_b32_e32 v5, 2, v5
	ds_bpermute_b32 v5, v5, v4
	v_max_f32_e32 v4, v4, v4
	v_cmp_lt_i32_e32 vcc, v51, v50
	v_mov_b32_e32 v50, v72
	s_waitcnt lgkmcnt(0)
	v_max_f32_e32 v5, v5, v5
	v_max_f32_e32 v4, v4, v5
	v_cndmask_b32_e32 v5, v242, v51, vcc
	v_lshlrev_b32_e32 v5, 2, v5
	ds_bpermute_b32 v5, v5, v4
	s_waitcnt lgkmcnt(0)
	v_max3_f32 v51, v73, v4, v5
	v_sub_f32_e32 v4, v73, v51
	v_exp_f32_e32 v78, v4
	v_mov_b64_e32 v[4:5], v[50:51]
	s_branch .LBB0_958

.LBB0_981:
	s_cmp_gt_i32 s8, s44
	s_cbranch_scc1 .LBB0_1001
	s_cmp_le_i32 s8, s9
	s_mul_hi_u32 s6, s52, 0xaaaaaaab
	s_cselect_b64 s[30:31], -1, 0
	s_lshr_b32 s34, s6, 1
	s_mul_i32 s34, s34, 0x18000
	v_add_u32_e32 v134, s8, v208
	v_subrev_u32_e32 v149, s34, v232
	v_subrev_u32_e32 v150, s34, v233
	v_subrev_u32_e32 v151, s34, v234
	v_subrev_u32_e32 v152, s34, v235
	v_lshl_or_b32 v188, s51, 6, v208
	s_mov_b64 s[18:19], -1
	s_and_b64 vcc, exec, s[30:31]
	v_add_u32_e32 v135, 4, v134
	v_or_b32_e32 v133, 6, v134
	v_or_b32_e32 v132, 2, v134
	v_add_u32_e32 v160, 3, v134
	v_add_u32_e32 v158, 5, v134
	v_add_u32_e32 v159, 7, v134
	v_or_b32_e32 v131, 36, v134
	v_or_b32_e32 v130, 32, v134
	v_or_b32_e32 v129, 37, v134
	v_or_b32_e32 v128, 33, v134
	v_or_b32_e32 v119, 38, v134
	v_or_b32_e32 v2, 34, v134
	s_cbranch_vccz .LBB0_988
	s_add_i32 s6, s45, s50
	v_add_u32_e32 v153, s6, v152
	v_add_u32_e32 v161, s6, v151
	v_add_u32_e32 v162, s6, v150
	v_add_u32_e32 v163, s6, v149
	ds_read_b128 v[46:49], v153
	ds_read_b128 v[50:53], v153 offset:4096
	ds_read_b128 v[120:123], v161
	ds_read_b128 v[124:127], v161 offset:4096
	ds_read_b128 v[136:139], v162
	ds_read_b128 v[140:143], v162 offset:4096
	ds_read_b128 v[144:147], v163
	ds_read_b128 v[154:157], v163 offset:4096
	s_waitcnt lgkmcnt(0)
	v_mfma_f32_16x16x32_f16 v[46:49], v[46:49], v[6:9], 0
	v_mfma_f32_16x16x32_f16 v[46:49], v[120:123], v[10:13], v[46:49]
	v_mfma_f32_16x16x32_f16 v[46:49], v[136:139], v[14:17], v[46:49]
	v_mfma_f32_16x16x32_f16 v[120:123], v[144:147], v[18:21], v[46:49]
	v_mfma_f32_16x16x32_f16 v[46:49], v[50:53], v[6:9], 0
	v_mfma_f32_16x16x32_f16 v[46:49], v[124:127], v[10:13], v[46:49]
	v_mfma_f32_16x16x32_f16 v[46:49], v[140:143], v[14:17], v[46:49]
	v_mfma_f32_16x16x32_f16 v[124:127], v[154:157], v[18:21], v[46:49]
	s_nop 5
	ds_read_b128 v[46:49], v153 offset:8192
	ds_read_b128 v[136:139], v153 offset:12288
	ds_read_b128 v[50:53], v161 offset:8192
	ds_read_b128 v[140:143], v161 offset:12288
	ds_read_b128 v[144:147], v162 offset:8192
	ds_read_b128 v[154:157], v162 offset:12288
	ds_read_b128 v[190:193], v163 offset:8192
	ds_read_b128 v[200:203], v163 offset:12288
	s_waitcnt lgkmcnt(0)
	v_mfma_f32_16x16x32_f16 v[46:49], v[46:49], v[6:9], 0
	v_mfma_f32_16x16x32_f16 v[46:49], v[50:53], v[10:13], v[46:49]
	v_mfma_f32_16x16x32_f16 v[46:49], v[144:147], v[14:17], v[46:49]
	v_mfma_f32_16x16x32_f16 v[50:53], v[190:193], v[18:21], v[46:49]
	v_mfma_f32_16x16x32_f16 v[46:49], v[136:139], v[6:9], 0
	v_mfma_f32_16x16x32_f16 v[46:49], v[140:143], v[10:13], v[46:49]
	v_mfma_f32_16x16x32_f16 v[46:49], v[154:157], v[14:17], v[46:49]
	v_mfma_f32_16x16x32_f16 v[46:49], v[200:203], v[18:21], v[46:49]
	v_lshlrev_b32_e32 v154, 4, v132
	v_lshlrev_b32_e32 v155, 4, v133
	v_lshlrev_b32_e32 v157, 4, v130
	v_add_u32_e32 v136, 0x270, v196
	v_add_u32_e32 v137, 0x260, v196
	v_sub_u32_e32 v138, v185, v154
	v_add_u32_e32 v139, 0x240, v196
	v_add_u32_e32 v140, 0x230, v196
	v_add_u32_e32 v141, 0x220, v196
	v_sub_u32_e32 v142, v185, v155
	v_add_u32_e32 v143, 0x200, v196
	v_sub_u32_e32 v144, v185, v157
	v_lshlrev_b32_e32 v161, 4, v128
	v_lshlrev_b32_e32 v163, 4, v2
	v_lshlrev_b32_e32 v186, 4, v131
	v_lshlrev_b32_e32 v187, 4, v129
	v_lshlrev_b32_e32 v189, 4, v119
	v_med3_i32 v136, v136, 31, v240
	v_med3_i32 v137, v137, 31, v240
	v_med3_i32 v138, v138, 31, v240
	v_med3_i32 v139, v139, 31, v240
	v_med3_i32 v140, v140, 31, v240
	v_med3_i32 v141, v141, 31, v240
	v_med3_i32 v142, v142, 31, v240
	v_med3_i32 v143, v143, 31, v240
	v_med3_i32 v144, v144, 31, v240
	v_sub_u32_e32 v145, v185, v161
	v_sub_u32_e32 v146, v185, v163
	v_add_u32_e32 v147, 64, v196
	v_sub_u32_e32 v153, v185, v186
	v_sub_u32_e32 v156, v185, v187
	v_sub_u32_e32 v162, v185, v189
	v_lshlrev_b32_e32 v136, 2, v136
	v_lshlrev_b32_e32 v137, 2, v137
	v_lshlrev_b32_e32 v138, 2, v138
	v_lshlrev_b32_e32 v139, 2, v139
	v_lshlrev_b32_e32 v140, 2, v140
	v_lshlrev_b32_e32 v141, 2, v141
	v_lshlrev_b32_e32 v142, 2, v142
	v_lshlrev_b32_e32 v143, 2, v143
	v_lshlrev_b32_e32 v144, 2, v144
	v_med3_i32 v145, v145, 31, v240
	v_med3_i32 v146, v146, 31, v240
	v_med3_i32 v147, v147, 31, v240
	v_med3_i32 v153, v153, 31, v240
	v_med3_i32 v156, v156, 31, v240
	v_med3_i32 v162, v162, 31, v240
	v_med3_i32 v168, v196, 31, v240
	v_add3_u32 v136, v244, v136, s59
	v_add3_u32 v137, v244, v137, s59
	v_add3_u32 v138, v244, v138, s59
	v_add3_u32 v139, v244, v139, s59
	v_add3_u32 v140, v244, v140, s59
	v_add3_u32 v141, v244, v141, s59
	v_add3_u32 v142, v244, v142, s59
	v_add3_u32 v143, v244, v143, s59
	v_add3_u32 v144, v244, v144, s59
	v_lshlrev_b32_e32 v145, 2, v145
	v_lshlrev_b32_e32 v146, 2, v146
	v_lshlrev_b32_e32 v147, 2, v147
	v_lshlrev_b32_e32 v153, 2, v153
	v_lshlrev_b32_e32 v156, 2, v156
	v_lshlrev_b32_e32 v162, 2, v162
	v_lshlrev_b32_e32 v168, 2, v168
	ds_read_b32 v136, v136
	ds_read_b32 v137, v137
	ds_read_b32 v138, v138
	ds_read_b32 v139, v139
	ds_read_b32 v140, v140
	ds_read_b32 v141, v141
	ds_read_b32 v142, v142
	ds_read_b32 v143, v143
	v_add3_u32 v145, v244, v145, s59
	v_add3_u32 v146, v244, v146, s59
	v_add3_u32 v147, v244, v147, s59
	v_add3_u32 v153, v244, v153, s59
	v_add3_u32 v156, v244, v156, s59
	v_add3_u32 v162, v244, v162, s59
	v_add3_u32 v168, v244, v168, s59
	ds_read_b32 v202, v144
	ds_read_b32 v201, v145
	ds_read_b32 v199, v146
	ds_read_b32 v200, v147
	ds_read_b32 v195, v153
	ds_read_b32 v194, v156
	ds_read_b32 v193, v162
	ds_read_b32 v192, v168
	v_add_u32_e32 v162, 3, v134
	v_add_u32_e32 v153, 5, v134
	v_add_u32_e32 v156, 7, v134
	s_waitcnt lgkmcnt(0)
	v_fmac_f32_e32 v137, 0x3e0293ee, v121
	v_sub_f32_e32 v121, v137, v4
	v_exp_f32_e32 v121, v121
	v_fmac_f32_e32 v136, 0x3e0293ee, v120
	v_fmac_f32_e32 v139, 0x3e0293ee, v123
	v_sub_f32_e32 v120, v136, v4
	v_mul_f32_e32 v136, v164, v121
	v_sub_f32_e32 v121, v139, v4
	v_exp_f32_e32 v121, v121
	v_cmp_le_i32_e32 vcc, v162, v172
	v_fmac_f32_e32 v141, 0x3e0293ee, v125
	v_fmac_f32_e32 v143, 0x3e0293ee, v127
	v_mul_f32_e32 v121, v164, v121
	v_cndmask_b32_e32 v190, 0, v121, vcc
	v_sub_f32_e32 v121, v141, v4
	v_exp_f32_e32 v123, v121
	v_fmac_f32_e32 v140, 0x3e0293ee, v124
	v_sub_f32_e32 v121, v140, v4
	v_exp_f32_e32 v120, v120
	v_mul_f32_e32 v137, v164, v123
	v_sub_f32_e32 v123, v143, v4
	v_exp_f32_e32 v124, v123
	v_exp_f32_e32 v121, v121
	v_fmac_f32_e32 v138, 0x3e0293ee, v122
	v_fmac_f32_e32 v142, 0x3e0293ee, v126
	v_sub_f32_e32 v122, v138, v4
	v_sub_f32_e32 v123, v142, v4
	v_exp_f32_e32 v122, v122
	v_exp_f32_e32 v123, v123
	v_mul_f32_e32 v124, v164, v124
	v_cmp_le_i32_e32 vcc, v156, v172
	v_pk_mul_f32 v[120:121], v[164:165], v[120:121]
	v_add_f32_dpp v142, v190, v190 quad_perm:[1,0,3,2] row_mask:0xf bank_mask:0xf bound_ctrl:1
	v_cndmask_b32_e32 v191, 0, v124, vcc
	v_cmp_le_i32_e32 vcc, v135, v167
	v_mov_b32_dpp v204, v142 quad_perm:[2,3,0,1] row_mask:0xf bank_mask:0xf bound_ctrl:1
	s_nop 0
	v_cndmask_b32_e32 v125, 0, v121, vcc
	v_cmp_le_i32_e32 vcc, v134, v172
	s_nop 1
	v_cndmask_b32_e32 v124, 0, v120, vcc
	v_cmp_ge_i32_e32 vcc, v172, v153
	v_pk_mul_f32 v[120:121], v[164:165], v[122:123]
	v_add_f32_dpp v123, v191, v191 quad_perm:[1,0,3,2] row_mask:0xf bank_mask:0xf bound_ctrl:1
	v_cndmask_b32_e32 v137, 0, v137, vcc
	v_cmp_lt_i32_e32 vcc, v134, v172
	v_add_f32_dpp v143, v123, v123 quad_perm:[2,3,0,1] row_mask:0xf bank_mask:0xf bound_ctrl:1
	ds_bpermute_b32 v203, v177, v143
	v_cndmask_b32_e32 v136, 0, v136, vcc
	v_cmp_le_i32_e32 vcc, v133, v167
	v_mov_b32_dpp v127, v137 quad_perm:[1,0,3,2] row_mask:0xf bank_mask:0xf bound_ctrl:1
	v_mov_b32_dpp v126, v136 quad_perm:[1,0,3,2] row_mask:0xf bank_mask:0xf bound_ctrl:1
	v_cndmask_b32_e32 v139, 0, v121, vcc
	v_cmp_le_i32_e32 vcc, v132, v172
	v_mov_b32_dpp v121, v125 quad_perm:[1,0,3,2] row_mask:0xf bank_mask:0xf bound_ctrl:1
	v_mov_b32_dpp v145, v139 quad_perm:[1,0,3,2] row_mask:0xf bank_mask:0xf bound_ctrl:1
	v_cndmask_b32_e32 v138, 0, v120, vcc
	v_mov_b32_dpp v120, v124 quad_perm:[1,0,3,2] row_mask:0xf bank_mask:0xf bound_ctrl:1
	v_pk_add_f32 v[120:121], v[124:125], v[120:121]
	v_mov_b32_dpp v144, v138 quad_perm:[1,0,3,2] row_mask:0xf bank_mask:0xf bound_ctrl:1
	v_pk_add_f32 v[126:127], v[136:137], v[126:127]
	v_pk_add_f32 v[144:145], v[138:139], v[144:145]
	v_mov_b32_dpp v122, v120 quad_perm:[2,3,0,1] row_mask:0xf bank_mask:0xf bound_ctrl:1
	v_mov_b32_dpp v140, v126 quad_perm:[2,3,0,1] row_mask:0xf bank_mask:0xf bound_ctrl:1
	v_mov_b32_dpp v146, v144 quad_perm:[2,3,0,1] row_mask:0xf bank_mask:0xf bound_ctrl:1
	v_mov_b32_dpp v123, v121 quad_perm:[2,3,0,1] row_mask:0xf bank_mask:0xf bound_ctrl:1
	v_mov_b32_dpp v141, v127 quad_perm:[2,3,0,1] row_mask:0xf bank_mask:0xf bound_ctrl:1
	v_mov_b32_dpp v147, v145 quad_perm:[2,3,0,1] row_mask:0xf bank_mask:0xf bound_ctrl:1
	s_and_saveexec_b64 s[6:7], s[4:5]
	s_cbranch_execz .LBB0_985
	v_pk_add_f32 v[126:127], v[126:127], v[140:141]
	v_pk_add_f32 v[120:121], v[120:121], v[122:123]
	v_pk_add_f32 v[144:145], v[144:145], v[146:147]
	v_pk_add_f32 v[120:121], v[120:121], v[126:127]
	s_waitcnt lgkmcnt(0)
	v_cndmask_b32_e64 v168, v203, v148, s[2:3]
	v_add_f32_e32 v169, v142, v204
	v_pk_add_f32 v[120:121], v[120:121], v[144:145]
	v_mov_b32_e32 v142, v169
	v_pk_fma_f32 v[120:121], v[120:121], 2.0, v[168:169] op_sel_hi:[1,0,1]
	v_add_u32_e32 v122, v236, v197
	v_pk_add_f32 v[120:121], v[142:143], v[120:121]
	ds_write_b64 v122, v[120:121]

.LBB0_990:
	s_add_i32 s35, s45, s50
	v_add_u32_e32 v50, s35, v152
	v_add_u32_e32 v51, s35, v151
	v_add_u32_e32 v144, s35, v150
	v_add_u32_e32 v145, s35, v149
	ds_read_b128 v[38:41], v50
	ds_read_b128 v[42:45], v50 offset:4096
	ds_read_b128 v[46:49], v51
	ds_read_b128 v[136:139], v51 offset:4096
	ds_read_b128 v[148:151], v144
	ds_read_b128 v[190:193], v144 offset:4096
	s_waitcnt lgkmcnt(0)
	ds_read_b128 v[200:203], v145
	ds_read_b128 v[204:207], v145 offset:4096
	v_mfma_f32_16x16x32_f16 v[38:41], v[38:41], v[22:25], 0
	v_mfma_f32_16x16x32_f16 v[38:41], v[46:49], v[26:29], v[38:41]
	v_mfma_f32_16x16x32_f16 v[38:41], v[148:151], v[30:33], v[38:41]
	s_waitcnt lgkmcnt(0)
	v_mfma_f32_16x16x32_f16 v[46:49], v[200:203], v[34:37], v[38:41]
	v_mfma_f32_16x16x32_f16 v[38:41], v[42:45], v[22:25], 0
	v_mfma_f32_16x16x32_f16 v[38:41], v[136:139], v[26:29], v[38:41]
	v_mfma_f32_16x16x32_f16 v[38:41], v[190:193], v[30:33], v[38:41]
	v_mfma_f32_16x16x32_f16 v[136:139], v[204:207], v[34:37], v[38:41]
	s_nop 5
	ds_read_b128 v[38:41], v50 offset:8192
	ds_read_b128 v[148:151], v50 offset:12288
	ds_read_b128 v[42:45], v51 offset:8192
	ds_read_b128 v[190:193], v51 offset:12288
	ds_read_b128 v[200:203], v144 offset:8192
	ds_read_b128 v[204:207], v144 offset:12288
	ds_read_b128 v[248:251], v145 offset:8192
	ds_read_b128 v[168:171], v145 offset:12288
	s_waitcnt lgkmcnt(0)
	v_mfma_f32_16x16x32_f16 v[38:41], v[38:41], v[22:25], 0
	v_mfma_f32_16x16x32_f16 v[38:41], v[42:45], v[26:29], v[38:41]
	v_mfma_f32_16x16x32_f16 v[38:41], v[200:203], v[30:33], v[38:41]
	v_mfma_f32_16x16x32_f16 v[42:45], v[248:251], v[34:37], v[38:41]
	v_mfma_f32_16x16x32_f16 v[38:41], v[148:151], v[22:25], 0
	v_mfma_f32_16x16x32_f16 v[38:41], v[190:193], v[26:29], v[38:41]
	v_mfma_f32_16x16x32_f16 v[38:41], v[204:207], v[30:33], v[38:41]
	v_mfma_f32_16x16x32_f16 v[38:41], v[168:171], v[34:37], v[38:41]
	v_add_u32_e32 v50, 0x274, v196
	v_add_u32_e32 v51, 0x264, v196
	v_sub_u32_e32 v144, v181, v154
	v_med3_i32 v50, v50, 31, v240
	v_med3_i32 v51, v51, 31, v240
	v_med3_i32 v144, v144, 31, v240
	v_sub_u32_e32 v143, v181, v143
	v_sub_u32_e32 v142, v181, v142
	v_sub_u32_e32 v141, v181, v141
	v_sub_u32_e32 v145, v181, v155
	v_sub_u32_e32 v140, v181, v140
	v_lshlrev_b32_e32 v50, 2, v50
	v_lshlrev_b32_e32 v51, 2, v51
	v_lshlrev_b32_e32 v144, 2, v144
	v_med3_i32 v143, v143, 31, v240
	v_med3_i32 v142, v142, 31, v240
	v_med3_i32 v141, v141, 31, v240
	v_med3_i32 v145, v145, 31, v240
	v_med3_i32 v140, v140, 31, v240
	v_add3_u32 v50, v244, v50, s59
	v_add3_u32 v51, v244, v51, s59
	v_add3_u32 v144, v244, v144, s59
	v_lshlrev_b32_e32 v143, 2, v143
	v_lshlrev_b32_e32 v142, 2, v142
	v_lshlrev_b32_e32 v141, 2, v141
	v_lshlrev_b32_e32 v145, 2, v145
	v_lshlrev_b32_e32 v140, 2, v140
	v_add3_u32 v143, v244, v143, s59
	v_add3_u32 v142, v244, v142, s59
	v_add3_u32 v141, v244, v141, s59
	v_add3_u32 v145, v244, v145, s59
	v_add3_u32 v140, v244, v140, s59
	ds_read_b32 v50, v50
	ds_read_b32 v51, v51
	ds_read_b32 v148, v144
	ds_read_b32 v151, v143
	ds_read_b32 v152, v142
	ds_read_b32 v154, v141
	ds_read_b32 v155, v145
	ds_read_b32 v158, v140
	v_sub_u32_e32 v144, v181, v187
	v_med3_i32 v144, v144, 31, v240
	v_sub_u32_e32 v140, v181, v157
	v_sub_u32_e32 v141, v181, v161
	v_sub_u32_e32 v142, v181, v163
	v_sub_u32_e32 v143, v181, v186
	v_lshlrev_b32_e32 v144, 2, v144
	v_med3_i32 v140, v140, 31, v240
	v_med3_i32 v141, v141, 31, v240
	v_med3_i32 v142, v142, 31, v240
	v_sub_u32_e32 v53, v181, v53
	v_med3_i32 v143, v143, 31, v240
	v_add3_u32 v157, v244, v144, s59
	v_sub_u32_e32 v144, v181, v189
	v_sub_u32_e32 v52, v181, v52
	v_lshlrev_b32_e32 v140, 2, v140
	v_lshlrev_b32_e32 v141, 2, v141
	v_lshlrev_b32_e32 v142, 2, v142
	v_med3_i32 v53, v53, 31, v240
	v_lshlrev_b32_e32 v143, 2, v143
	v_med3_i32 v144, v144, 31, v240
	v_med3_i32 v52, v52, 31, v240
	v_add3_u32 v140, v244, v140, s59
	v_add3_u32 v141, v244, v141, s59
	v_add3_u32 v142, v244, v142, s59
	v_lshlrev_b32_e32 v53, 2, v53
	v_add3_u32 v143, v244, v143, s59
	v_lshlrev_b32_e32 v144, 2, v144
	v_lshlrev_b32_e32 v52, 2, v52
	v_add3_u32 v53, v244, v53, s59
	v_add3_u32 v159, v244, v144, s59
	v_add3_u32 v52, v244, v52, s59
	ds_read_b32 v150, v140
	ds_read_b32 v149, v141
	ds_read_b32 v144, v142
	ds_read_b32 v145, v53
	ds_read_b32 v143, v143
	ds_read_b32 v142, v157
	ds_read_b32 v141, v159
	ds_read_b32 v140, v52
	s_waitcnt lgkmcnt(0)
	v_fmac_f32_e32 v51, 0x3e0293ee, v47
	v_sub_f32_e32 v47, v51, v5
	v_exp_f32_e32 v47, v47
	v_fmac_f32_e32 v50, 0x3e0293ee, v46
	v_fmac_f32_e32 v151, 0x3e0293ee, v49
	v_sub_f32_e32 v46, v50, v5
	v_mul_f32_e32 v50, v182, v47
	v_sub_f32_e32 v47, v151, v5
	v_exp_f32_e32 v47, v47
	v_cmp_le_i32_e32 vcc, v162, v184
	v_fmac_f32_e32 v154, 0x3e0293ee, v137
	v_fmac_f32_e32 v158, 0x3e0293ee, v139
	v_mul_f32_e32 v47, v182, v47
	v_cndmask_b32_e32 v200, 0, v47, vcc
	v_sub_f32_e32 v47, v154, v5
	v_exp_f32_e32 v49, v47
	v_fmac_f32_e32 v152, 0x3e0293ee, v136
	v_sub_f32_e32 v47, v152, v5
	v_exp_f32_e32 v46, v46
	v_mul_f32_e32 v51, v182, v49
	v_sub_f32_e32 v49, v158, v5
	v_exp_f32_e32 v52, v49
	v_exp_f32_e32 v47, v47
	v_fmac_f32_e32 v148, 0x3e0293ee, v48
	v_fmac_f32_e32 v155, 0x3e0293ee, v138
	v_sub_f32_e32 v48, v148, v5
	v_sub_f32_e32 v49, v155, v5
	v_mul_f32_e32 v52, v182, v52
	v_cmp_le_i32_e32 vcc, v156, v184
	v_exp_f32_e32 v48, v48
	v_exp_f32_e32 v49, v49
	v_cndmask_b32_e32 v201, 0, v52, vcc
	v_pk_mul_f32 v[46:47], v[182:183], v[46:47]
	v_cmp_le_i32_e32 vcc, v135, v1
	v_pk_mul_f32 v[48:49], v[182:183], v[48:49]
	v_add_f32_dpp v152, v200, v200 quad_perm:[1,0,3,2] row_mask:0xf bank_mask:0xf bound_ctrl:1
	v_cndmask_b32_e32 v47, 0, v47, vcc
	v_cmp_le_i32_e32 vcc, v134, v184
	v_mov_b32_dpp v154, v152 quad_perm:[2,3,0,1] row_mask:0xf bank_mask:0xf bound_ctrl:1
	v_add_u32_e32 v148, v236, v197
	v_cndmask_b32_e32 v46, 0, v46, vcc
	v_cmp_ge_i32_e32 vcc, v184, v153
	s_nop 1
	v_cndmask_b32_e32 v187, 0, v51, vcc
	v_cmp_lt_i32_e32 vcc, v134, v184
	v_add_f32_dpp v51, v201, v201 quad_perm:[1,0,3,2] row_mask:0xf bank_mask:0xf bound_ctrl:1
	v_mov_b32_dpp v53, v187 quad_perm:[1,0,3,2] row_mask:0xf bank_mask:0xf bound_ctrl:1
	v_cndmask_b32_e32 v186, 0, v50, vcc
	v_cmp_le_i32_e32 vcc, v133, v1
	s_nop 0
	v_mov_b32_dpp v52, v186 quad_perm:[1,0,3,2] row_mask:0xf bank_mask:0xf bound_ctrl:1
	v_cndmask_b32_e32 v189, 0, v49, vcc
	v_cmp_le_i32_e32 vcc, v132, v184
	v_mov_b32_dpp v49, v47 quad_perm:[1,0,3,2] row_mask:0xf bank_mask:0xf bound_ctrl:1
	v_mov_b32_dpp v135, v189 quad_perm:[1,0,3,2] row_mask:0xf bank_mask:0xf bound_ctrl:1
	v_cndmask_b32_e32 v188, 0, v48, vcc
	v_mov_b32_dpp v48, v46 quad_perm:[1,0,3,2] row_mask:0xf bank_mask:0xf bound_ctrl:1
	v_pk_add_f32 v[48:49], v[46:47], v[48:49]
	v_mov_b32_dpp v134, v188 quad_perm:[1,0,3,2] row_mask:0xf bank_mask:0xf bound_ctrl:1
	v_pk_add_f32 v[136:137], v[188:189], v[134:135]
	v_add_f32_dpp v135, v51, v51 quad_perm:[2,3,0,1] row_mask:0xf bank_mask:0xf bound_ctrl:1
	ds_bpermute_b32 v151, v177, v135
	v_pk_add_f32 v[52:53], v[186:187], v[52:53]
	v_mov_b32_dpp v50, v48 quad_perm:[2,3,0,1] row_mask:0xf bank_mask:0xf bound_ctrl:1
	v_mov_b32_dpp v138, v136 quad_perm:[2,3,0,1] row_mask:0xf bank_mask:0xf bound_ctrl:1
	v_mov_b32_dpp v132, v52 quad_perm:[2,3,0,1] row_mask:0xf bank_mask:0xf bound_ctrl:1
	v_mov_b32_dpp v51, v49 quad_perm:[2,3,0,1] row_mask:0xf bank_mask:0xf bound_ctrl:1
	v_mov_b32_dpp v133, v53 quad_perm:[2,3,0,1] row_mask:0xf bank_mask:0xf bound_ctrl:1
	v_mov_b32_dpp v139, v137 quad_perm:[2,3,0,1] row_mask:0xf bank_mask:0xf bound_ctrl:1
	s_and_saveexec_b64 s[6:7], s[4:5]
	s_cbranch_execz .LBB0_992
	v_pk_add_f32 v[52:53], v[52:53], v[132:133]
	v_pk_add_f32 v[48:49], v[48:49], v[50:51]
	v_pk_add_f32 v[136:137], v[136:137], v[138:139]
	v_pk_add_f32 v[48:49], v[48:49], v[52:53]
	s_waitcnt lgkmcnt(0)
	v_cndmask_b32_e64 v156, v151, v118, s[2:3]
	v_add_f32_e32 v157, v152, v154
	v_pk_add_f32 v[48:49], v[48:49], v[136:137]
	v_mov_b32_e32 v134, v157
	v_pk_fma_f32 v[48:49], v[48:49], 2.0, v[156:157] op_sel_hi:[1,0,1]
	s_nop 0
	v_pk_add_f32 v[48:49], v[134:135], v[48:49]
	ds_write_b64 v148, v[48:49] offset:2048

.LBB0_1133:
	s_waitcnt lgkmcnt(0)
	s_sub_i32 s6, s96, 64
	s_lshr_b64 s[18:19], s[26:27], s96
	s_lshr_b64 s[20:21], s[28:29], s6
	s_lshr_b64 s[34:35], s[22:23], s96
	s_lshr_b64 s[38:39], s[24:25], s6
	s_cmp_lt_u32 s96, 64
	s_cselect_b64 s[0:1], -1, 0
	s_and_b64 s[42:43], s[0:1], exec
	s_cselect_b32 s7, s18, s20
	s_cselect_b32 s20, s34, s38
	s_bitcmp1_b32 s7, 0
	s_cselect_b64 s[18:19], -1, 0
	s_bitcmp1_b32 s20, 0
	s_cselect_b64 s[76:77], -1, 0
	s_or_b64 s[20:21], s[18:19], s[76:77]
	s_andn2_b64 vcc, exec, s[20:21]
	s_cbranch_vccnz .LBB0_1139
	v_lshrrev_b64 v[118:119], s96, v[200:201]
	v_lshrrev_b64 v[120:121], s6, v[202:203]
	v_cndmask_b32_e64 v2, v120, v118, s[0:1]
	v_lshrrev_b64 v[118:119], s96, v[196:197]
	v_lshrrev_b64 v[120:121], s6, v[198:199]
	v_cndmask_b32_e64 v1, v120, v118, s[0:1]
	s_mul_hi_u32 s0, s50, 0xaaaaaaab
	s_lshr_b32 s34, s0, 1
	s_and_b64 s[6:7], s[18:19], s[76:77]
	s_cmpk_lt_i32 s45, 0x7f
	s_cselect_b64 s[0:1], -1, 0
	s_cmpk_gt_i32 s45, 0x7e
	s_cselect_b64 s[20:21], -1, 0
	s_mul_i32 s34, s34, 0x18000
	s_and_b64 s[20:21], s[20:21], s[6:7]
	v_cndmask_b32_e64 v5, 0, 1, s[18:19]
	v_subrev_u32_e32 v142, s34, v232
	v_subrev_u32_e32 v143, s34, v233
	v_subrev_u32_e32 v144, s34, v234
	v_subrev_u32_e32 v145, s34, v235
	s_mov_b64 s[6:7], -1
	s_andn2_b64 vcc, exec, s[20:21]
	v_cmp_ne_u32_e64 s[18:19], 1, v5
	s_cbranch_vccz .LBB0_1160
	s_and_b64 vcc, exec, s[18:19]
	v_mov_b64_e32 v[204:205], v[136:137]
	v_mov_b64_e32 v[206:207], v[134:135]
	s_cbranch_vccnz .LBB0_1147
	s_add_i32 s6, s9, s8
	v_add_u32_e32 v5, s6, v145
	v_add_u32_e32 v150, s6, v144
	v_add_u32_e32 v151, s6, v143
	v_add_u32_e32 v154, s6, v142
	ds_read_b128 v[38:41], v5
	ds_read_b128 v[42:45], v5 offset:4096
	ds_read_b128 v[118:121], v150
	ds_read_b128 v[122:125], v150 offset:4096
	ds_read_b128 v[126:129], v151
	ds_read_b128 v[138:141], v151 offset:4096
	ds_read_b128 v[130:133], v154
	ds_read_b128 v[146:149], v154 offset:4096
	s_waitcnt lgkmcnt(0)
	v_mfma_f32_16x16x32_f16 v[38:41], v[38:41], v[6:9], 0
	v_mfma_f32_16x16x32_f16 v[38:41], v[118:121], v[10:13], v[38:41]
	v_mfma_f32_16x16x32_f16 v[38:41], v[126:129], v[14:17], v[38:41]
	v_mfma_f32_16x16x32_f16 v[130:133], v[130:133], v[18:21], v[38:41]
	v_mfma_f32_16x16x32_f16 v[38:41], v[42:45], v[6:9], 0
	v_mfma_f32_16x16x32_f16 v[38:41], v[122:125], v[10:13], v[38:41]
	v_mfma_f32_16x16x32_f16 v[38:41], v[138:141], v[14:17], v[38:41]
	v_mfma_f32_16x16x32_f16 v[126:129], v[146:149], v[18:21], v[38:41]
	s_nop 5
	ds_read_b128 v[38:41], v5 offset:8192
	ds_read_b128 v[42:45], v5 offset:12288
	ds_read_b128 v[118:121], v150 offset:8192
	ds_read_b128 v[138:141], v150 offset:12288
	ds_read_b128 v[122:125], v151 offset:8192
	ds_read_b128 v[146:149], v151 offset:12288
	ds_read_b128 v[150:153], v154 offset:8192
	ds_read_b128 v[154:157], v154 offset:12288
	s_waitcnt lgkmcnt(0)
	v_mfma_f32_16x16x32_f16 v[38:41], v[38:41], v[6:9], 0
	v_mfma_f32_16x16x32_f16 v[38:41], v[118:121], v[10:13], v[38:41]
	v_mfma_f32_16x16x32_f16 v[38:41], v[122:125], v[14:17], v[38:41]
	v_mfma_f32_16x16x32_f16 v[122:125], v[150:153], v[18:21], v[38:41]
	v_mfma_f32_16x16x32_f16 v[38:41], v[42:45], v[6:9], 0
	v_mfma_f32_16x16x32_f16 v[38:41], v[138:141], v[10:13], v[38:41]
	v_mfma_f32_16x16x32_f16 v[38:41], v[146:149], v[14:17], v[38:41]
	v_mfma_f32_16x16x32_f16 v[118:121], v[154:157], v[18:21], v[38:41]
	s_mov_b64 s[6:7], -1
	s_and_b64 vcc, exec, s[0:1]
	s_cbranch_vccz .LBB0_1142
	v_add_u32_e32 v5, s45, v238
	s_nop 1
	v_add_u32_e32 v38, 63, v5
	v_add_u32_e32 v40, 62, v5
	v_add_u32_e32 v42, 61, v5
	v_add_u32_e32 v44, 60, v5
	v_add_u32_e32 v138, 59, v5
	v_add_u32_e32 v140, 58, v5
	v_add_u32_e32 v146, 57, v5
	v_add_u32_e32 v148, 56, v5
	v_add_u32_e32 v150, 31, v5
	v_add_u32_e32 v152, 30, v5
	v_add_u32_e32 v154, 29, v5
	v_add_u32_e32 v156, 28, v5
	v_add_u32_e32 v158, 27, v5
	v_add_u32_e32 v160, 26, v5
	v_add_u32_e32 v162, 25, v5
	v_med3_i32 v39, v38, 0, v243
	v_med3_i32 v41, v40, 0, v243
	v_med3_i32 v43, v42, 0, v243
	v_med3_i32 v45, v44, 0, v243
	v_med3_i32 v139, v138, 0, v243
	v_med3_i32 v141, v140, 0, v243
	v_med3_i32 v147, v146, 0, v243
	v_med3_i32 v149, v148, 0, v243
	v_med3_i32 v151, v150, 0, v243
	v_med3_i32 v153, v152, 0, v243
	v_med3_i32 v155, v154, 0, v243
	v_med3_i32 v157, v156, 0, v243
	v_med3_i32 v159, v158, 0, v243
	v_med3_i32 v161, v160, 0, v243
	v_med3_i32 v163, v162, 0, v243
	v_add_u32_e32 v164, 24, v5
	v_lshl_add_u32 v39, v39, 2, v244
	v_lshl_add_u32 v41, v41, 2, v244
	v_lshl_add_u32 v43, v43, 2, v244
	v_lshl_add_u32 v45, v45, 2, v244
	v_lshl_add_u32 v139, v139, 2, v244
	v_lshl_add_u32 v141, v141, 2, v244
	v_lshl_add_u32 v147, v147, 2, v244
	v_lshl_add_u32 v149, v149, 2, v244
	v_lshl_add_u32 v151, v151, 2, v244
	v_lshl_add_u32 v153, v153, 2, v244
	v_lshl_add_u32 v155, v155, 2, v244
	v_lshl_add_u32 v157, v157, 2, v244
	v_lshl_add_u32 v159, v159, 2, v244
	v_lshl_add_u32 v161, v161, 2, v244
	v_lshl_add_u32 v163, v163, 2, v244
	v_med3_i32 v5, v164, 0, v243
	ds_read_b32 v39, v39
	ds_read_b32 v41, v41
	ds_read_b32 v43, v43
	ds_read_b32 v45, v45
	ds_read_b32 v139, v139
	ds_read_b32 v141, v141
	ds_read_b32 v147, v147
	ds_read_b32 v149, v149
	v_lshl_add_u32 v5, v5, 2, v244
	ds_read_b32 v151, v151
	ds_read_b32 v153, v153
	ds_read_b32 v155, v155
	ds_read_b32 v157, v157
	ds_read_b32 v159, v159
	ds_read_b32 v161, v161
	ds_read_b32 v163, v163
	ds_read_b32 v165, v5
	v_and_b32_e32 v5, 1, v2
	v_cmp_eq_u32_e32 vcc, 1, v5
	v_cmp_lt_i32_e64 s[0:1], -1, v38
	s_waitcnt lgkmcnt(0)
	v_fmac_f32_e32 v39, 0x3e0293ee, v130
	s_and_b64 s[0:1], s[0:1], vcc
	v_cndmask_b32_e64 v5, v241, v39, s[0:1]
	v_cmp_lt_i32_e64 s[0:1], -1, v40
	v_fmac_f32_e32 v41, 0x3e0293ee, v131
	s_and_b64 s[0:1], s[0:1], vcc
	v_cndmask_b32_e64 v38, v241, v41, s[0:1]
	v_cmp_lt_i32_e64 s[0:1], -1, v42
	v_fmac_f32_e32 v43, 0x3e0293ee, v132
	s_and_b64 s[0:1], s[0:1], vcc
	v_cndmask_b32_e64 v39, v241, v43, s[0:1]
	v_cmp_lt_i32_e64 s[0:1], -1, v44
	v_fmac_f32_e32 v45, 0x3e0293ee, v133
	s_and_b64 s[0:1], s[0:1], vcc
	v_cndmask_b32_e64 v41, v241, v45, s[0:1]
	v_cmp_lt_i32_e64 s[0:1], -1, v138
	v_fmac_f32_e32 v139, 0x3e0293ee, v126
	s_and_b64 s[0:1], s[0:1], vcc
	v_cndmask_b32_e64 v40, v241, v139, s[0:1]
	v_cmp_lt_i32_e64 s[0:1], -1, v140
	v_fmac_f32_e32 v141, 0x3e0293ee, v127
	s_and_b64 s[0:1], s[0:1], vcc
	v_cndmask_b32_e64 v140, v241, v141, s[0:1]
	v_cmp_lt_i32_e64 s[0:1], -1, v146
	v_fmac_f32_e32 v147, 0x3e0293ee, v128
	s_and_b64 s[0:1], s[0:1], vcc
	v_cndmask_b32_e64 v147, v241, v147, s[0:1]
	v_cmp_lt_i32_e64 s[0:1], -1, v148
	v_fmac_f32_e32 v149, 0x3e0293ee, v129
	s_and_b64 s[0:1], s[0:1], vcc
	v_cndmask_b32_e64 v149, v241, v149, s[0:1]
	v_cmp_lt_i32_e64 s[0:1], -1, v150
	v_fmac_f32_e32 v151, 0x3e0293ee, v122
	s_and_b64 s[0:1], s[0:1], vcc
	v_cndmask_b32_e64 v44, v241, v151, s[0:1]
	v_cmp_lt_i32_e64 s[0:1], -1, v152
	v_fmac_f32_e32 v153, 0x3e0293ee, v123
	s_and_b64 s[0:1], s[0:1], vcc
	v_cndmask_b32_e64 v45, v241, v153, s[0:1]
	v_cmp_lt_i32_e64 s[0:1], -1, v154
	v_fmac_f32_e32 v155, 0x3e0293ee, v124
	s_and_b64 s[0:1], s[0:1], vcc
	v_cndmask_b32_e64 v138, v241, v155, s[0:1]
	v_cmp_lt_i32_e64 s[0:1], -1, v156
	v_fmac_f32_e32 v157, 0x3e0293ee, v125
	s_and_b64 s[0:1], s[0:1], vcc
	v_cndmask_b32_e64 v141, v241, v157, s[0:1]
	v_cmp_lt_i32_e64 s[0:1], -1, v158
	v_fmac_f32_e32 v159, 0x3e0293ee, v118
	s_and_b64 s[0:1], s[0:1], vcc
	v_cndmask_b32_e64 v139, v241, v159, s[0:1]
	v_cmp_lt_i32_e64 s[0:1], -1, v160
	v_max_f32_e32 v42, v5, v38
	v_fmac_f32_e32 v161, 0x3e0293ee, v119
	s_and_b64 s[0:1], s[0:1], vcc
	v_max3_f32 v42, v42, v39, v41
	v_cndmask_b32_e64 v146, v241, v161, s[0:1]
	v_cmp_lt_i32_e64 s[0:1], -1, v162
	v_max3_f32 v42, v42, v40, v140
	v_fmac_f32_e32 v163, 0x3e0293ee, v120
	s_and_b64 s[0:1], s[0:1], vcc
	v_max3_f32 v42, v42, v147, v149
	v_cndmask_b32_e64 v148, v241, v163, s[0:1]
	v_cmp_lt_i32_e64 s[0:1], -1, v164
	v_max3_f32 v42, v42, v44, v45
	v_fmac_f32_e32 v165, 0x3e0293ee, v121
	s_and_b64 vcc, s[0:1], vcc
	v_max3_f32 v42, v42, v138, v141
	v_cndmask_b32_e32 v150, v241, v165, vcc
	v_max3_f32 v42, v42, v139, v146
	v_max3_f32 v42, v42, v148, v150
	v_add_f32_e32 v43, 0x41000000, v136
	v_cmp_gt_f32_e32 vcc, v42, v43
	s_cbranch_vccz .LBB0_1140
	ds_bpermute_b32 v43, v245, v42
	v_max_f32_e32 v42, v42, v42
	s_waitcnt lgkmcnt(0)
	v_max_f32_e32 v43, v43, v43
	v_max_f32_e32 v42, v42, v43
	ds_bpermute_b32 v43, v246, v42
	s_waitcnt lgkmcnt(0)
	v_max3_f32 v42, v136, v42, v43
	v_sub_f32_e32 v43, v136, v42
	v_exp_f32_e32 v194, v43
	v_mov_b32_e32 v43, v137
	v_mov_b64_e32 v[204:205], v[42:43]
	s_branch .LBB0_1141

.LBB0_1147:
	s_andn2_b64 vcc, exec, s[76:77]
	s_cbranch_vccnz .LBB0_1159
	s_add_i32 s0, s9, s8
	v_add_u32_e32 v4, s0, v145
	v_add_u32_e32 v5, s0, v144
	v_add_u32_e32 v150, s0, v143
	v_add_u32_e32 v154, s0, v142
	ds_read_b128 v[46:49], v4
	ds_read_b128 v[50:53], v4 offset:4096
	ds_read_b128 v[118:121], v5
	ds_read_b128 v[122:125], v5 offset:4096
	ds_read_b128 v[126:129], v150
	ds_read_b128 v[138:141], v150 offset:4096
	ds_read_b128 v[130:133], v154
	ds_read_b128 v[146:149], v154 offset:4096
	s_waitcnt lgkmcnt(0)
	v_mfma_f32_16x16x32_f16 v[46:49], v[46:49], v[22:25], 0
	v_mfma_f32_16x16x32_f16 v[46:49], v[118:121], v[26:29], v[46:49]
	v_mfma_f32_16x16x32_f16 v[46:49], v[126:129], v[30:33], v[46:49]
	v_mfma_f32_16x16x32_f16 v[130:133], v[130:133], v[34:37], v[46:49]
	v_mfma_f32_16x16x32_f16 v[46:49], v[50:53], v[22:25], 0
	v_mfma_f32_16x16x32_f16 v[46:49], v[122:125], v[26:29], v[46:49]
	v_mfma_f32_16x16x32_f16 v[46:49], v[138:141], v[30:33], v[46:49]
	v_mfma_f32_16x16x32_f16 v[126:129], v[146:149], v[34:37], v[46:49]
	s_nop 5
	ds_read_b128 v[46:49], v4 offset:8192
	ds_read_b128 v[50:53], v4 offset:12288
	ds_read_b128 v[118:121], v5 offset:8192
	ds_read_b128 v[138:141], v5 offset:12288
	ds_read_b128 v[122:125], v150 offset:8192
	ds_read_b128 v[146:149], v150 offset:12288
	ds_read_b128 v[150:153], v154 offset:8192
	ds_read_b128 v[154:157], v154 offset:12288
	s_waitcnt lgkmcnt(0)
	v_mfma_f32_16x16x32_f16 v[46:49], v[46:49], v[22:25], 0
	v_mfma_f32_16x16x32_f16 v[46:49], v[118:121], v[26:29], v[46:49]
	v_mfma_f32_16x16x32_f16 v[46:49], v[122:125], v[30:33], v[46:49]
	v_mfma_f32_16x16x32_f16 v[122:125], v[150:153], v[34:37], v[46:49]
	v_mfma_f32_16x16x32_f16 v[46:49], v[50:53], v[22:25], 0
	v_mfma_f32_16x16x32_f16 v[46:49], v[138:141], v[26:29], v[46:49]
	v_mfma_f32_16x16x32_f16 v[46:49], v[146:149], v[30:33], v[46:49]
	v_mfma_f32_16x16x32_f16 v[118:121], v[154:157], v[34:37], v[46:49]
	s_add_i32 s0, s45, 4
	s_cmpk_gt_i32 s0, 0x7e
	s_mov_b64 s[0:1], -1
	s_cbranch_scc1 .LBB0_1153
	v_add_u32_e32 v4, s45, v238
	s_nop 0
	v_add_u32_e32 v48, 0x43, v4
	v_max_i32_e32 v46, 1, v48
	v_max_i32_e32 v47, 2, v48
	v_max_i32_e32 v49, 3, v48
	v_max_i32_e32 v50, 4, v48
	v_add_u32_e32 v46, -1, v46
	v_add_u32_e32 v47, -2, v47
	v_add_u32_e32 v49, -3, v49
	v_add_u32_e32 v50, -4, v50
	v_add_u32_e32 v51, 62, v4
	v_add_u32_e32 v53, 61, v4
	v_add_u32_e32 v139, 60, v4
	v_add_u32_e32 v141, 35, v4
	v_add_u32_e32 v147, 34, v4
	v_add_u32_e32 v150, 33, v4
	v_add_u32_e32 v152, 32, v4
	v_add_u32_e32 v153, 31, v4
	v_add_u32_e32 v155, 30, v4
	v_add_u32_e32 v157, 29, v4
	v_add_u32_e32 v4, 28, v4
	v_med3_i32 v5, v48, 0, v243
	v_min_u32_e32 v46, 0x7f, v46
	v_min_u32_e32 v47, 0x7f, v47
	v_min_u32_e32 v49, 0x7f, v49
	v_min_u32_e32 v50, 0x7f, v50
	v_med3_i32 v52, v51, 0, v243
	v_med3_i32 v138, v53, 0, v243
	v_med3_i32 v140, v139, 0, v243
	v_med3_i32 v146, v141, 0, v243
	v_med3_i32 v148, v147, 0, v243
	v_med3_i32 v154, v153, 0, v243
	v_med3_i32 v156, v155, 0, v243
	v_med3_i32 v158, v157, 0, v243
	v_med3_i32 v159, v4, 0, v243
	v_lshl_add_u32 v5, v5, 2, v244
	v_lshl_add_u32 v46, v46, 2, v244
	v_lshl_add_u32 v47, v47, 2, v244
	v_lshl_add_u32 v49, v49, 2, v244
	v_lshl_add_u32 v50, v50, 2, v244
	v_lshl_add_u32 v52, v52, 2, v244
	v_lshl_add_u32 v138, v138, 2, v244
	v_lshl_add_u32 v140, v140, 2, v244
	v_lshl_add_u32 v146, v146, 2, v244
	v_lshl_add_u32 v148, v148, 2, v244
	v_med3_i32 v149, v150, 0, v243
	v_med3_i32 v151, v152, 0, v243
	v_lshl_add_u32 v154, v154, 2, v244
	v_lshl_add_u32 v156, v156, 2, v244
	v_lshl_add_u32 v158, v158, 2, v244
	v_lshl_add_u32 v159, v159, 2, v244
	ds_read_b32 v5, v5
	ds_read_b32 v46, v46
	ds_read_b32 v47, v47
	ds_read_b32 v49, v49
	ds_read_b32 v50, v50
	ds_read_b32 v52, v52
	ds_read_b32 v138, v138
	ds_read_b32 v140, v140
	v_lshl_add_u32 v149, v149, 2, v244
	v_lshl_add_u32 v151, v151, 2, v244
	ds_read_b32 v160, v146
	ds_read_b32 v148, v148
	ds_read_b32 v161, v149
	ds_read_b32 v162, v151
	ds_read_b32 v154, v154
	ds_read_b32 v156, v156
	ds_read_b32 v158, v158
	ds_read_b32 v159, v159
	v_and_b32_e32 v146, 1, v1
	v_cmp_eq_u32_e32 vcc, 1, v146
	v_cmp_lt_i32_e64 s[0:1], -1, v48
	s_waitcnt lgkmcnt(0)
	v_fmac_f32_e32 v5, 0x3e0293ee, v130
	s_and_b64 s[0:1], s[0:1], vcc
	v_cndmask_b32_e64 v5, v241, v5, s[0:1]
	v_cmp_lt_i32_e64 s[0:1], 0, v48
	v_fmac_f32_e32 v46, 0x3e0293ee, v131
	s_and_b64 s[0:1], s[0:1], vcc
	v_cndmask_b32_e64 v46, v241, v46, s[0:1]
	v_cmp_lt_i32_e64 s[0:1], 1, v48
	v_fmac_f32_e32 v47, 0x3e0293ee, v132
	s_and_b64 s[0:1], s[0:1], vcc
	v_cndmask_b32_e64 v47, v241, v47, s[0:1]
	v_cmp_lt_i32_e64 s[0:1], 2, v48
	v_fmac_f32_e32 v49, 0x3e0293ee, v133
	s_and_b64 s[0:1], s[0:1], vcc
	v_cndmask_b32_e64 v49, v241, v49, s[0:1]
	v_cmp_lt_i32_e64 s[0:1], 3, v48
	v_fmac_f32_e32 v50, 0x3e0293ee, v126
	s_and_b64 s[0:1], s[0:1], vcc
	v_cndmask_b32_e64 v48, v241, v50, s[0:1]
	v_cmp_lt_i32_e64 s[0:1], -1, v51
	v_fmac_f32_e32 v52, 0x3e0293ee, v127
	s_and_b64 s[0:1], s[0:1], vcc
	v_cndmask_b32_e64 v146, v241, v52, s[0:1]
	v_cmp_lt_i32_e64 s[0:1], -1, v53
	v_fmac_f32_e32 v138, 0x3e0293ee, v128
	s_and_b64 s[0:1], s[0:1], vcc
	v_cndmask_b32_e64 v149, v241, v138, s[0:1]
	v_cmp_lt_i32_e64 s[0:1], -1, v139
	v_fmac_f32_e32 v140, 0x3e0293ee, v129
	s_and_b64 s[0:1], s[0:1], vcc
	v_cndmask_b32_e64 v151, v241, v140, s[0:1]
	v_cmp_lt_i32_e64 s[0:1], -1, v141
	v_fmac_f32_e32 v160, 0x3e0293ee, v122
	s_and_b64 s[0:1], s[0:1], vcc
	v_cndmask_b32_e64 v52, v241, v160, s[0:1]
	v_cmp_lt_i32_e64 s[0:1], -1, v147
	v_fmac_f32_e32 v148, 0x3e0293ee, v123
	s_and_b64 s[0:1], s[0:1], vcc
	v_cndmask_b32_e64 v53, v241, v148, s[0:1]
	v_cmp_lt_i32_e64 s[0:1], -1, v150
	v_fmac_f32_e32 v161, 0x3e0293ee, v124
	s_and_b64 s[0:1], s[0:1], vcc
	v_cndmask_b32_e64 v140, v241, v161, s[0:1]
	v_cmp_lt_i32_e64 s[0:1], -1, v152
	v_fmac_f32_e32 v162, 0x3e0293ee, v125
	s_and_b64 s[0:1], s[0:1], vcc
	v_cndmask_b32_e64 v147, v241, v162, s[0:1]
	v_cmp_lt_i32_e64 s[0:1], -1, v153
	v_fmac_f32_e32 v154, 0x3e0293ee, v118
	s_and_b64 s[0:1], s[0:1], vcc
	v_cndmask_b32_e64 v141, v241, v154, s[0:1]
	v_cmp_lt_i32_e64 s[0:1], -1, v155
	v_fmac_f32_e32 v156, 0x3e0293ee, v119
	s_and_b64 s[0:1], s[0:1], vcc
	v_cndmask_b32_e64 v148, v241, v156, s[0:1]
	v_cmp_lt_i32_e64 s[0:1], -1, v157
	v_fmac_f32_e32 v158, 0x3e0293ee, v120
	s_and_b64 s[0:1], s[0:1], vcc
	v_cndmask_b32_e64 v150, v241, v158, s[0:1]
	v_cmp_lt_i32_e64 s[0:1], -1, v4
	v_max_f32_e32 v4, v5, v46
	v_max3_f32 v4, v4, v47, v49
	v_max3_f32 v4, v4, v48, v146
	v_max3_f32 v4, v4, v149, v151
	v_max3_f32 v4, v4, v52, v53
	v_fmac_f32_e32 v159, 0x3e0293ee, v121
	s_and_b64 vcc, s[0:1], vcc
	v_max3_f32 v4, v4, v140, v147
	v_cndmask_b32_e32 v152, v241, v159, vcc
	v_max3_f32 v4, v4, v141, v148
	v_max3_f32 v4, v4, v150, v152
	v_add_f32_e32 v50, 0x41000000, v205
	v_cmp_gt_f32_e32 vcc, v4, v50
	s_cbranch_vccz .LBB0_1151
	ds_bpermute_b32 v50, v245, v4
	v_max_f32_e32 v4, v4, v4
	s_waitcnt lgkmcnt(0)
	v_max_f32_e32 v50, v50, v50
	v_max_f32_e32 v4, v4, v50
	ds_bpermute_b32 v50, v246, v4
	s_waitcnt lgkmcnt(0)
	v_max3_f32 v51, v205, v4, v50
	v_sub_f32_e32 v4, v205, v51
	v_exp_f32_e32 v4, v4
	v_mov_b32_e32 v50, v204
	v_mov_b64_e32 v[138:139], v[50:51]
	s_branch .LBB0_1152

.LBB0_1160:
	s_and_b64 vcc, exec, s[6:7]
	s_cbranch_vccz .LBB0_1167
	s_add_i32 s0, s9, s8
	v_add_u32_e32 v4, s0, v145
	v_add_u32_e32 v5, s0, v144
	v_add_u32_e32 v130, s0, v143
	v_add_u32_e32 v131, s0, v142
	ds_read_b128 v[38:41], v4
	ds_read_b128 v[42:45], v4 offset:4096
	ds_read_b128 v[46:49], v5
	ds_read_b128 v[50:53], v5 offset:4096
	ds_read_b128 v[118:121], v130
	ds_read_b128 v[126:129], v130 offset:4096
	ds_read_b128 v[122:125], v131
	ds_read_b128 v[138:141], v131 offset:4096
	ds_read_b128 v[142:145], v4 offset:8192
	ds_read_b128 v[146:149], v4 offset:12288
	ds_read_b128 v[150:153], v5 offset:8192
	ds_read_b128 v[154:157], v5 offset:12288
	ds_read_b128 v[158:161], v130 offset:8192
	ds_read_b128 v[162:165], v130 offset:12288
	ds_read_b128 v[168:171], v131 offset:8192
	ds_read_b128 v[204:207], v131 offset:12288
	s_waitcnt lgkmcnt(8)
	s_waitcnt lgkmcnt(0)
	v_mfma_f32_16x16x32_f16 v[130:133], v[38:41], v[6:9], 0
	v_mfma_f32_16x16x32_f16 v[38:41], v[38:41], v[22:25], 0
	v_mfma_f32_16x16x32_f16 v[130:133], v[46:49], v[10:13], v[130:133]
	v_mfma_f32_16x16x32_f16 v[38:41], v[46:49], v[26:29], v[38:41]
	v_mfma_f32_16x16x32_f16 v[46:49], v[118:121], v[14:17], v[130:133]
	v_mfma_f32_16x16x32_f16 v[38:41], v[118:121], v[30:33], v[38:41]
	v_mfma_f32_16x16x32_f16 v[130:133], v[122:125], v[18:21], v[46:49]
	v_mfma_f32_16x16x32_f16 v[122:125], v[122:125], v[34:37], v[38:41]
	v_mfma_f32_16x16x32_f16 v[38:41], v[42:45], v[6:9], 0
	v_mfma_f32_16x16x32_f16 v[42:45], v[42:45], v[22:25], 0
	v_mfma_f32_16x16x32_f16 v[38:41], v[50:53], v[10:13], v[38:41]
	v_mfma_f32_16x16x32_f16 v[42:45], v[50:53], v[26:29], v[42:45]
	v_mfma_f32_16x16x32_f16 v[38:41], v[126:129], v[14:17], v[38:41]
	v_mfma_f32_16x16x32_f16 v[42:45], v[126:129], v[30:33], v[42:45]
	v_mfma_f32_16x16x32_f16 v[38:41], v[138:141], v[18:21], v[38:41]
	v_mfma_f32_16x16x32_f16 v[46:49], v[138:141], v[34:37], v[42:45]
	v_mfma_f32_16x16x32_f16 v[42:45], v[142:145], v[6:9], 0
	v_mfma_f32_16x16x32_f16 v[50:53], v[142:145], v[22:25], 0
	v_mfma_f32_16x16x32_f16 v[42:45], v[150:153], v[10:13], v[42:45]
	v_mfma_f32_16x16x32_f16 v[50:53], v[150:153], v[26:29], v[50:53]
	v_mfma_f32_16x16x32_f16 v[42:45], v[158:161], v[14:17], v[42:45]
	v_mfma_f32_16x16x32_f16 v[50:53], v[158:161], v[30:33], v[50:53]
	v_mfma_f32_16x16x32_f16 v[126:129], v[168:171], v[18:21], v[42:45]
	v_mfma_f32_16x16x32_f16 v[118:121], v[168:171], v[34:37], v[50:53]
	v_mfma_f32_16x16x32_f16 v[42:45], v[146:149], v[6:9], 0
	v_mfma_f32_16x16x32_f16 v[50:53], v[146:149], v[22:25], 0
	v_mfma_f32_16x16x32_f16 v[42:45], v[154:157], v[10:13], v[42:45]
	v_mfma_f32_16x16x32_f16 v[50:53], v[154:157], v[26:29], v[50:53]
	v_mfma_f32_16x16x32_f16 v[42:45], v[162:165], v[14:17], v[42:45]
	v_mfma_f32_16x16x32_f16 v[50:53], v[162:165], v[30:33], v[50:53]
	v_mfma_f32_16x16x32_f16 v[42:45], v[204:207], v[18:21], v[42:45]
	v_mfma_f32_16x16x32_f16 v[50:53], v[204:207], v[34:37], v[50:53]
	v_max_f32_e32 v4, v131, v131
	v_max_f32_e32 v5, v130, v130
	v_max_f32_e32 v4, v5, v4
	v_max3_f32 v4, v4, v132, v133
	v_max3_f32 v4, v4, v38, v39
	v_max3_f32 v4, v4, v40, v41
	v_max3_f32 v4, v4, v126, v127
	v_max3_f32 v4, v4, v128, v129
	v_and_b32_e32 v2, 1, v2
	v_max3_f32 v4, v4, v42, v43
	v_max3_f32 v4, v4, v44, v45
	v_cmp_eq_u32_e32 vcc, 1, v2
	v_mul_f32_e32 v172, 0x3e0293ee, v4
	v_mov_b32_e32 v143, v136
	v_cndmask_b32_e32 v142, v241, v180, vcc
	v_pk_add_f32 v[138:139], v[142:143], v[172:173]
	v_mov_b32_e32 v4, 1.0
	v_cmp_gt_f32_e32 vcc, v138, v139
	s_cbranch_vccz .LBB0_1163
	ds_bpermute_b32 v2, v245, v138
	v_max_f32_e32 v5, v138, v138
	v_mov_b32_e32 v139, v137
	s_waitcnt lgkmcnt(0)
	v_max_f32_e32 v2, v2, v2
	v_max_f32_e32 v2, v5, v2
	ds_bpermute_b32 v5, v246, v2
	s_waitcnt lgkmcnt(0)
	v_max3_f32 v138, v136, v2, v5
	v_sub_f32_e32 v2, v136, v138
	v_exp_f32_e32 v194, v2
	v_mov_b32_e32 v136, v138
	s_branch .LBB0_1164

.LBB0_1203:
	s_waitcnt lgkmcnt(0)
	s_add_i32 s34, s10, 63
	s_cmp_le_i32 s10, s9
	s_cselect_b64 s[6:7], -1, 0
	s_cmp_ge_i32 s34, s17
	s_cselect_b64 s[18:19], -1, 0
	s_and_b64 s[18:19], s[6:7], s[18:19]
	s_cmp_le_i32 s10, s8
	s_cselect_b64 s[20:21], -1, 0
	s_cmp_ge_i32 s34, s44
	s_cselect_b64 s[6:7], -1, 0
	s_and_b64 s[36:37], s[20:21], s[6:7]
	s_or_b64 s[20:21], s[18:19], s[36:37]
	s_andn2_b64 vcc, exec, s[20:21]
	s_cbranch_vccnz .LBB0_1209
	s_mul_hi_u32 s20, s13, 0xaaaaaaab
	s_lshr_b32 s42, s20, 1
	s_and_b64 s[6:7], s[18:19], s[6:7]
	s_add_i32 s20, s14, 0xffffffba
	s_cmpk_gt_i32 s20, 0x7e
	s_cselect_b64 s[34:35], -1, 0
	s_and_b64 s[6:7], s[34:35], s[6:7]
	s_cmpk_lt_i32 s14, 0x200
	s_cselect_b64 s[20:21], -1, 0
	s_mul_i32 s42, s42, 0x18000
	s_and_b64 s[38:39], s[6:7], s[20:21]
	v_cndmask_b32_e64 v5, 0, 1, s[18:19]
	v_subrev_u32_e32 v1, s42, v232
	v_subrev_u32_e32 v2, s42, v233
	v_subrev_u32_e32 v142, s42, v234
	v_subrev_u32_e32 v143, s42, v235
	s_mov_b64 s[6:7], -1
	s_andn2_b64 vcc, exec, s[38:39]
	v_cmp_ne_u32_e64 s[18:19], 1, v5
	s_cbranch_vccz .LBB0_1230
	s_and_b64 vcc, exec, s[18:19]
	v_mov_b64_e32 v[196:197], v[136:137]
	v_mov_b64_e32 v[198:199], v[134:135]
	s_cbranch_vccnz .LBB0_1217
	s_add_i32 s6, s15, s47
	v_add_u32_e32 v5, s6, v143
	v_add_u32_e32 v148, s6, v142
	v_add_u32_e32 v149, s6, v2
	v_add_u32_e32 v152, s6, v1
	ds_read_b128 v[38:41], v5
	ds_read_b128 v[42:45], v5 offset:4096
	ds_read_b128 v[118:121], v148
	ds_read_b128 v[122:125], v148 offset:4096
	ds_read_b128 v[126:129], v149
	ds_read_b128 v[138:141], v149 offset:4096
	ds_read_b128 v[130:133], v152
	ds_read_b128 v[144:147], v152 offset:4096
	s_waitcnt lgkmcnt(0)
	v_mfma_f32_16x16x32_f16 v[38:41], v[38:41], v[6:9], 0
	v_mfma_f32_16x16x32_f16 v[38:41], v[118:121], v[10:13], v[38:41]
	v_mfma_f32_16x16x32_f16 v[38:41], v[126:129], v[14:17], v[38:41]
	v_mfma_f32_16x16x32_f16 v[130:133], v[130:133], v[18:21], v[38:41]
	v_mfma_f32_16x16x32_f16 v[38:41], v[42:45], v[6:9], 0
	v_mfma_f32_16x16x32_f16 v[38:41], v[122:125], v[10:13], v[38:41]
	v_mfma_f32_16x16x32_f16 v[38:41], v[138:141], v[14:17], v[38:41]
	v_mfma_f32_16x16x32_f16 v[126:129], v[144:147], v[18:21], v[38:41]
	s_nop 5
	ds_read_b128 v[38:41], v5 offset:8192
	ds_read_b128 v[42:45], v5 offset:12288
	ds_read_b128 v[118:121], v148 offset:8192
	ds_read_b128 v[138:141], v148 offset:12288
	ds_read_b128 v[122:125], v149 offset:8192
	ds_read_b128 v[144:147], v149 offset:12288
	ds_read_b128 v[148:151], v152 offset:8192
	ds_read_b128 v[152:155], v152 offset:12288
	s_waitcnt lgkmcnt(0)
	v_mfma_f32_16x16x32_f16 v[38:41], v[38:41], v[6:9], 0
	v_mfma_f32_16x16x32_f16 v[38:41], v[118:121], v[10:13], v[38:41]
	v_mfma_f32_16x16x32_f16 v[38:41], v[122:125], v[14:17], v[38:41]
	v_mfma_f32_16x16x32_f16 v[122:125], v[148:151], v[18:21], v[38:41]
	v_mfma_f32_16x16x32_f16 v[38:41], v[42:45], v[6:9], 0
	v_mfma_f32_16x16x32_f16 v[38:41], v[138:141], v[10:13], v[38:41]
	v_mfma_f32_16x16x32_f16 v[38:41], v[144:147], v[14:17], v[38:41]
	v_mfma_f32_16x16x32_f16 v[118:121], v[152:155], v[18:21], v[38:41]
	s_add_i32 s6, s14, -4
	s_cmpk_lt_i32 s6, 0x200
	s_cselect_b64 s[6:7], -1, 0
	s_and_b64 s[6:7], s[34:35], s[6:7]
	s_andn2_b64 vcc, exec, s[6:7]
	s_mov_b64 s[6:7], -1
	s_cbranch_vccz .LBB0_1212
	v_add_u32_e32 v5, s14, v239
	v_add_u32_e32 v38, -7, v5
	v_add_u32_e32 v40, -8, v5
	v_add_u32_e32 v42, -9, v5
	v_add_u32_e32 v44, -10, v5
	v_add_u32_e32 v138, -11, v5
	v_add_u32_e32 v140, -12, v5
	v_add_u32_e32 v144, -13, v5
	v_med3_i32 v39, v38, 0, v243
	v_med3_i32 v41, v40, 0, v243
	v_med3_i32 v43, v42, 0, v243
	v_med3_i32 v45, v44, 0, v243
	v_med3_i32 v139, v138, 0, v243
	v_med3_i32 v141, v140, 0, v243
	v_med3_i32 v145, v144, 0, v243
	v_add_u32_e32 v148, -14, v5
	v_lshl_add_u32 v39, v39, 2, v244
	v_lshl_add_u32 v41, v41, 2, v244
	v_lshl_add_u32 v43, v43, 2, v244
	v_lshl_add_u32 v45, v45, 2, v244
	v_lshl_add_u32 v139, v139, 2, v244
	v_lshl_add_u32 v141, v141, 2, v244
	v_lshl_add_u32 v145, v145, 2, v244
	v_med3_i32 v146, v148, 0, v243
	v_subrev_u32_e32 v150, 39, v5
	v_subrev_u32_e32 v152, 41, v5
	v_subrev_u32_e32 v154, 42, v5
	v_subrev_u32_e32 v156, 43, v5
	v_subrev_u32_e32 v158, 44, v5
	v_subrev_u32_e32 v160, 45, v5
	v_lshl_add_u32 v146, v146, 2, v244
	ds_read_b32 v39, v39
	ds_read_b32 v41, v41
	ds_read_b32 v43, v43
	ds_read_b32 v45, v45
	ds_read_b32 v139, v139
	ds_read_b32 v141, v141
	ds_read_b32 v147, v145
	ds_read_b32 v149, v146
	v_med3_i32 v145, v150, 0, v243
	v_subrev_u32_e32 v151, 40, v5
	v_med3_i32 v153, v152, 0, v243
	v_med3_i32 v155, v154, 0, v243
	v_med3_i32 v157, v156, 0, v243
	v_med3_i32 v159, v158, 0, v243
	v_med3_i32 v161, v160, 0, v243
	v_subrev_u32_e32 v162, 46, v5
	v_lshl_add_u32 v145, v145, 2, v244
	v_med3_i32 v146, v151, 0, v243
	v_lshl_add_u32 v153, v153, 2, v244
	v_lshl_add_u32 v155, v155, 2, v244
	v_lshl_add_u32 v157, v157, 2, v244
	v_lshl_add_u32 v159, v159, 2, v244
	v_lshl_add_u32 v161, v161, 2, v244
	v_med3_i32 v5, v162, 0, v243
	v_lshl_add_u32 v146, v146, 2, v244
	v_lshl_add_u32 v5, v5, 2, v244
	ds_read_b32 v163, v145
	ds_read_b32 v164, v146
	ds_read_b32 v153, v153
	ds_read_b32 v155, v155
	ds_read_b32 v157, v157
	ds_read_b32 v159, v159
	ds_read_b32 v161, v161
	ds_read_b32 v165, v5
	s_waitcnt lgkmcnt(0)
	v_fmac_f32_e32 v39, 0x3e0293ee, v130
	v_cmp_gt_u32_e32 vcc, s62, v38
	v_fmac_f32_e32 v41, 0x3e0293ee, v131
	v_fmac_f32_e32 v43, 0x3e0293ee, v132
	v_cndmask_b32_e32 v38, v241, v39, vcc
	v_cmp_gt_u32_e32 vcc, s62, v40
	v_fmac_f32_e32 v45, 0x3e0293ee, v133
	v_fmac_f32_e32 v139, 0x3e0293ee, v126
	v_cndmask_b32_e32 v39, v241, v41, vcc
	v_cmp_gt_u32_e32 vcc, s62, v42
	v_fmac_f32_e32 v141, 0x3e0293ee, v127
	v_fmac_f32_e32 v147, 0x3e0293ee, v128
	v_cndmask_b32_e32 v41, v241, v43, vcc
	v_cmp_gt_u32_e32 vcc, s62, v44
	v_fmac_f32_e32 v149, 0x3e0293ee, v129
	v_fmac_f32_e32 v163, 0x3e0293ee, v122
	v_cndmask_b32_e32 v146, v241, v45, vcc
	v_cmp_gt_u32_e32 vcc, s62, v138
	v_fmac_f32_e32 v164, 0x3e0293ee, v123
	v_fmac_f32_e32 v153, 0x3e0293ee, v124
	v_cndmask_b32_e32 v40, v241, v139, vcc
	v_cmp_gt_u32_e32 vcc, s62, v140
	v_max_f32_e32 v42, v38, v39
	v_fmac_f32_e32 v155, 0x3e0293ee, v125
	v_cndmask_b32_e32 v145, v241, v141, vcc
	v_cmp_gt_u32_e32 vcc, s62, v144
	v_max3_f32 v42, v42, v41, v146
	v_fmac_f32_e32 v157, 0x3e0293ee, v118
	v_cndmask_b32_e32 v147, v241, v147, vcc
	v_cmp_gt_u32_e32 vcc, s62, v148
	v_max3_f32 v42, v42, v40, v145
	v_fmac_f32_e32 v159, 0x3e0293ee, v119
	v_cndmask_b32_e32 v148, v241, v149, vcc
	v_cmp_gt_u32_e32 vcc, s62, v150
	v_max3_f32 v42, v42, v147, v148
	v_fmac_f32_e32 v161, 0x3e0293ee, v120
	v_cndmask_b32_e32 v5, v241, v163, vcc
	v_cmp_gt_u32_e32 vcc, s62, v151
	v_fmac_f32_e32 v165, 0x3e0293ee, v121
	v_add_f32_e32 v43, 0x41000000, v136
	v_cndmask_b32_e32 v44, v241, v164, vcc
	v_cmp_gt_u32_e32 vcc, s62, v152
	v_max3_f32 v42, v42, v5, v44
	s_nop 0
	v_cndmask_b32_e32 v138, v241, v153, vcc
	v_cmp_gt_u32_e32 vcc, s62, v154
	s_nop 1
	v_cndmask_b32_e32 v140, v241, v155, vcc
	v_cmp_gt_u32_e32 vcc, s62, v156
	v_max3_f32 v42, v42, v138, v140
	s_nop 0
	v_cndmask_b32_e32 v45, v241, v157, vcc
	v_cmp_gt_u32_e32 vcc, s62, v158
	s_nop 1
	v_cndmask_b32_e32 v139, v241, v159, vcc
	v_cmp_gt_u32_e32 vcc, s62, v160
	v_max3_f32 v42, v42, v45, v139
	s_nop 0
	v_cndmask_b32_e32 v141, v241, v161, vcc
	v_cmp_gt_u32_e32 vcc, s62, v162
	s_nop 1
	v_cndmask_b32_e32 v144, v241, v165, vcc
	v_max3_f32 v42, v42, v141, v144
	v_cmp_gt_f32_e32 vcc, v42, v43
	s_cbranch_vccz .LBB0_1210
	ds_bpermute_b32 v43, v245, v42
	v_max_f32_e32 v42, v42, v42
	s_waitcnt lgkmcnt(0)
	v_max_f32_e32 v43, v43, v43
	v_max_f32_e32 v42, v42, v43
	ds_bpermute_b32 v43, v246, v42
	s_waitcnt lgkmcnt(0)
	v_max3_f32 v42, v136, v42, v43
	v_sub_f32_e32 v43, v136, v42
	v_exp_f32_e32 v194, v43
	v_mov_b32_e32 v43, v137
	v_mov_b64_e32 v[196:197], v[42:43]
	s_branch .LBB0_1211

.LBB0_1217:
	s_andn2_b64 vcc, exec, s[36:37]
	s_cbranch_vccnz .LBB0_1229
	s_add_i32 s6, s15, s47
	v_add_u32_e32 v4, s6, v143
	v_add_u32_e32 v5, s6, v142
	v_add_u32_e32 v148, s6, v2
	v_add_u32_e32 v152, s6, v1
	ds_read_b128 v[46:49], v4
	ds_read_b128 v[50:53], v4 offset:4096
	ds_read_b128 v[118:121], v5
	ds_read_b128 v[122:125], v5 offset:4096
	ds_read_b128 v[126:129], v148
	ds_read_b128 v[138:141], v148 offset:4096
	ds_read_b128 v[130:133], v152
	ds_read_b128 v[144:147], v152 offset:4096
	s_waitcnt lgkmcnt(0)
	v_mfma_f32_16x16x32_f16 v[46:49], v[46:49], v[22:25], 0
	v_mfma_f32_16x16x32_f16 v[46:49], v[118:121], v[26:29], v[46:49]
	v_mfma_f32_16x16x32_f16 v[46:49], v[126:129], v[30:33], v[46:49]
	v_mfma_f32_16x16x32_f16 v[130:133], v[130:133], v[34:37], v[46:49]
	v_mfma_f32_16x16x32_f16 v[46:49], v[50:53], v[22:25], 0
	v_mfma_f32_16x16x32_f16 v[46:49], v[122:125], v[26:29], v[46:49]
	v_mfma_f32_16x16x32_f16 v[46:49], v[138:141], v[30:33], v[46:49]
	v_mfma_f32_16x16x32_f16 v[126:129], v[144:147], v[34:37], v[46:49]
	s_nop 5
	ds_read_b128 v[46:49], v4 offset:8192
	ds_read_b128 v[50:53], v4 offset:12288
	ds_read_b128 v[118:121], v5 offset:8192
	ds_read_b128 v[138:141], v5 offset:12288
	ds_read_b128 v[122:125], v148 offset:8192
	ds_read_b128 v[144:147], v148 offset:12288
	ds_read_b128 v[148:151], v152 offset:8192
	ds_read_b128 v[152:155], v152 offset:12288
	s_waitcnt lgkmcnt(0)
	v_mfma_f32_16x16x32_f16 v[46:49], v[46:49], v[22:25], 0
	v_mfma_f32_16x16x32_f16 v[46:49], v[118:121], v[26:29], v[46:49]
	v_mfma_f32_16x16x32_f16 v[46:49], v[122:125], v[30:33], v[46:49]
	v_mfma_f32_16x16x32_f16 v[122:125], v[148:151], v[34:37], v[46:49]
	v_mfma_f32_16x16x32_f16 v[46:49], v[50:53], v[22:25], 0
	v_mfma_f32_16x16x32_f16 v[46:49], v[138:141], v[26:29], v[46:49]
	v_mfma_f32_16x16x32_f16 v[46:49], v[144:147], v[30:33], v[46:49]
	v_mfma_f32_16x16x32_f16 v[118:121], v[152:155], v[34:37], v[46:49]
	s_add_i32 s6, s14, 0xffffffbe
	s_cmpk_gt_i32 s6, 0x7e
	s_cselect_b64 s[6:7], -1, 0
	s_and_b64 s[20:21], s[6:7], s[20:21]
	s_mov_b64 s[6:7], -1
	s_and_b64 vcc, exec, s[20:21]
	s_cbranch_vccnz .LBB0_1223
	v_add_u32_e32 v4, s14, v239
	v_add_u32_e32 v5, -3, v4
	v_max_i32_e32 v47, 1, v5
	v_add_u32_e32 v47, -1, v47
	v_add_u32_e32 v48, -5, v4
	v_add_u32_e32 v50, -6, v4
	v_add_u32_e32 v52, -7, v4
	v_add_u32_e32 v138, -8, v4
	v_add_u32_e32 v140, -9, v4
	v_add_u32_e32 v144, -10, v4
	v_subrev_u32_e32 v146, 35, v4
	v_subrev_u32_e32 v151, 36, v4
	v_subrev_u32_e32 v152, 37, v4
	v_subrev_u32_e32 v153, 38, v4
	v_subrev_u32_e32 v154, 39, v4
	v_subrev_u32_e32 v156, 40, v4
	v_subrev_u32_e32 v158, 41, v4
	v_subrev_u32_e32 v4, 42, v4
	v_med3_i32 v46, v5, 0, v243
	v_min_u32_e32 v47, 0x7f, v47
	v_med3_i32 v49, v48, 0, v243
	v_med3_i32 v51, v50, 0, v243
	v_med3_i32 v53, v52, 0, v243
	v_med3_i32 v139, v138, 0, v243
	v_med3_i32 v141, v140, 0, v243
	v_med3_i32 v145, v144, 0, v243
	v_med3_i32 v147, v146, 0, v243
	v_med3_i32 v155, v154, 0, v243
	v_med3_i32 v157, v156, 0, v243
	v_med3_i32 v159, v158, 0, v243
	v_med3_i32 v160, v4, 0, v243
	v_lshl_add_u32 v46, v46, 2, v244
	v_lshl_add_u32 v47, v47, 2, v244
	v_lshl_add_u32 v49, v49, 2, v244
	v_lshl_add_u32 v51, v51, 2, v244
	v_lshl_add_u32 v53, v53, 2, v244
	v_lshl_add_u32 v139, v139, 2, v244
	v_lshl_add_u32 v141, v141, 2, v244
	v_lshl_add_u32 v145, v145, 2, v244
	v_lshl_add_u32 v147, v147, 2, v244
	v_med3_i32 v148, v151, 0, v243
	v_med3_i32 v149, v152, 0, v243
	v_med3_i32 v150, v153, 0, v243
	v_lshl_add_u32 v155, v155, 2, v244
	v_lshl_add_u32 v157, v157, 2, v244
	v_lshl_add_u32 v159, v159, 2, v244
	v_lshl_add_u32 v160, v160, 2, v244
	ds_read_b32 v46, v46
	ds_read_b32 v47, v47
	ds_read_b32 v49, v49
	ds_read_b32 v51, v51
	ds_read_b32 v53, v53
	ds_read_b32 v139, v139
	ds_read_b32 v141, v141
	ds_read_b32 v145, v145
	v_lshl_add_u32 v148, v148, 2, v244
	v_lshl_add_u32 v149, v149, 2, v244
	v_lshl_add_u32 v150, v150, 2, v244
	ds_read_b32 v161, v147
	ds_read_b32 v162, v148
	ds_read_b32 v163, v149
	ds_read_b32 v164, v150
	ds_read_b32 v155, v155
	ds_read_b32 v157, v157
	ds_read_b32 v159, v159
	ds_read_b32 v160, v160
	s_waitcnt lgkmcnt(0)
	v_fmac_f32_e32 v46, 0x3e0293ee, v130
	v_cmp_gt_u32_e32 vcc, s62, v5
	s_movk_i32 s6, 0x201
	v_fmac_f32_e32 v47, 0x3e0293ee, v131
	v_cndmask_b32_e32 v46, v241, v46, vcc
	v_cmp_gt_u32_e32 vcc, s6, v5
	v_fmac_f32_e32 v49, 0x3e0293ee, v132
	v_fmac_f32_e32 v51, 0x3e0293ee, v133
	v_cndmask_b32_e32 v47, v241, v47, vcc
	v_cmp_gt_u32_e32 vcc, s62, v48
	v_fmac_f32_e32 v53, 0x3e0293ee, v126
	v_fmac_f32_e32 v139, 0x3e0293ee, v127
	v_cndmask_b32_e32 v49, v241, v49, vcc
	v_cmp_gt_u32_e32 vcc, s62, v50
	v_fmac_f32_e32 v141, 0x3e0293ee, v128
	v_fmac_f32_e32 v145, 0x3e0293ee, v129
	v_cndmask_b32_e32 v148, v241, v51, vcc
	v_cmp_gt_u32_e32 vcc, s62, v52
	v_fmac_f32_e32 v161, 0x3e0293ee, v122
	v_fmac_f32_e32 v162, 0x3e0293ee, v123
	v_cndmask_b32_e32 v48, v241, v53, vcc
	v_cmp_gt_u32_e32 vcc, s62, v138
	v_fmac_f32_e32 v163, 0x3e0293ee, v124
	v_fmac_f32_e32 v164, 0x3e0293ee, v125
	v_cndmask_b32_e32 v147, v241, v139, vcc
	v_cmp_gt_u32_e32 vcc, s62, v140
	v_fmac_f32_e32 v155, 0x3e0293ee, v118
	v_fmac_f32_e32 v157, 0x3e0293ee, v119
	v_cndmask_b32_e32 v149, v241, v141, vcc
	v_cmp_gt_u32_e32 vcc, s62, v144
	v_fmac_f32_e32 v159, 0x3e0293ee, v120
	v_fmac_f32_e32 v160, 0x3e0293ee, v121
	v_cndmask_b32_e32 v150, v241, v145, vcc
	v_cmp_gt_u32_e32 vcc, s62, v146
	v_add_f32_e32 v50, 0x41000000, v197
	s_nop 0
	v_cndmask_b32_e32 v5, v241, v161, vcc
	v_cmp_gt_u32_e32 vcc, s62, v151
	s_nop 1
	v_cndmask_b32_e32 v52, v241, v162, vcc
	v_cmp_gt_u32_e32 vcc, s62, v152
	s_nop 1
	v_cndmask_b32_e32 v140, v241, v163, vcc
	v_cmp_gt_u32_e32 vcc, s62, v153
	s_nop 1
	v_cndmask_b32_e32 v144, v241, v164, vcc
	v_cmp_gt_u32_e32 vcc, s62, v154
	s_nop 1
	v_cndmask_b32_e32 v53, v241, v155, vcc
	v_cmp_gt_u32_e32 vcc, s62, v156
	s_nop 1
	v_cndmask_b32_e32 v141, v241, v157, vcc
	v_cmp_gt_u32_e32 vcc, s62, v158
	s_nop 1
	v_cndmask_b32_e32 v145, v241, v159, vcc
	v_cmp_gt_u32_e32 vcc, s62, v4
	v_max_f32_e32 v4, v46, v47
	v_max3_f32 v4, v4, v49, v148
	v_max3_f32 v4, v4, v48, v147
	v_max3_f32 v4, v4, v149, v150
	v_max3_f32 v4, v4, v5, v52
	v_max3_f32 v4, v4, v140, v144
	v_cndmask_b32_e32 v146, v241, v160, vcc
	v_max3_f32 v4, v4, v53, v141
	v_max3_f32 v4, v4, v145, v146
	v_cmp_gt_f32_e32 vcc, v4, v50
	s_cbranch_vccz .LBB0_1221
	ds_bpermute_b32 v50, v245, v4
	v_max_f32_e32 v4, v4, v4
	s_waitcnt lgkmcnt(0)
	v_max_f32_e32 v50, v50, v50
	v_max_f32_e32 v4, v4, v50
	ds_bpermute_b32 v50, v246, v4
	s_waitcnt lgkmcnt(0)
	v_max3_f32 v51, v197, v4, v50
	v_sub_f32_e32 v4, v197, v51
	v_exp_f32_e32 v4, v4
	v_mov_b32_e32 v50, v196
	v_mov_b64_e32 v[138:139], v[50:51]
	s_branch .LBB0_1222

.LBB0_1230:
	s_and_b64 vcc, exec, s[6:7]
	s_cbranch_vccz .LBB0_1237
	s_add_i32 s6, s15, s47
	v_add_u32_e32 v4, s6, v143
	v_add_u32_e32 v5, s6, v142
	v_add_u32_e32 v2, s6, v2
	v_add_u32_e32 v1, s6, v1
	ds_read_b128 v[38:41], v4
	ds_read_b128 v[42:45], v4 offset:4096
	ds_read_b128 v[46:49], v5
	ds_read_b128 v[50:53], v5 offset:4096
	ds_read_b128 v[118:121], v2
	ds_read_b128 v[126:129], v2 offset:4096
	ds_read_b128 v[122:125], v1
	ds_read_b128 v[138:141], v1 offset:4096
	ds_read_b128 v[142:145], v4 offset:8192
	ds_read_b128 v[146:149], v4 offset:12288
	ds_read_b128 v[150:153], v5 offset:8192
	ds_read_b128 v[154:157], v5 offset:12288
	ds_read_b128 v[158:161], v2 offset:8192
	ds_read_b128 v[162:165], v2 offset:12288
	ds_read_b128 v[168:171], v1 offset:8192
	ds_read_b128 v[194:197], v1 offset:12288
	s_waitcnt lgkmcnt(8)
	s_waitcnt lgkmcnt(0)
	v_mfma_f32_16x16x32_f16 v[130:133], v[38:41], v[6:9], 0
	v_mfma_f32_16x16x32_f16 v[38:41], v[38:41], v[22:25], 0
	v_mfma_f32_16x16x32_f16 v[130:133], v[46:49], v[10:13], v[130:133]
	v_mfma_f32_16x16x32_f16 v[38:41], v[46:49], v[26:29], v[38:41]
	v_mfma_f32_16x16x32_f16 v[46:49], v[118:121], v[14:17], v[130:133]
	v_mfma_f32_16x16x32_f16 v[38:41], v[118:121], v[30:33], v[38:41]
	v_mfma_f32_16x16x32_f16 v[130:133], v[122:125], v[18:21], v[46:49]
	v_mfma_f32_16x16x32_f16 v[122:125], v[122:125], v[34:37], v[38:41]
	v_mfma_f32_16x16x32_f16 v[38:41], v[42:45], v[6:9], 0
	v_mfma_f32_16x16x32_f16 v[42:45], v[42:45], v[22:25], 0
	v_mfma_f32_16x16x32_f16 v[38:41], v[50:53], v[10:13], v[38:41]
	v_mfma_f32_16x16x32_f16 v[42:45], v[50:53], v[26:29], v[42:45]
	v_mfma_f32_16x16x32_f16 v[38:41], v[126:129], v[14:17], v[38:41]
	v_mfma_f32_16x16x32_f16 v[42:45], v[126:129], v[30:33], v[42:45]
	v_mfma_f32_16x16x32_f16 v[38:41], v[138:141], v[18:21], v[38:41]
	v_mfma_f32_16x16x32_f16 v[46:49], v[138:141], v[34:37], v[42:45]
	v_mfma_f32_16x16x32_f16 v[42:45], v[142:145], v[6:9], 0
	v_mfma_f32_16x16x32_f16 v[50:53], v[142:145], v[22:25], 0
	v_mfma_f32_16x16x32_f16 v[42:45], v[150:153], v[10:13], v[42:45]
	v_mfma_f32_16x16x32_f16 v[50:53], v[150:153], v[26:29], v[50:53]
	v_mfma_f32_16x16x32_f16 v[42:45], v[158:161], v[14:17], v[42:45]
	v_mfma_f32_16x16x32_f16 v[50:53], v[158:161], v[30:33], v[50:53]
	v_mfma_f32_16x16x32_f16 v[126:129], v[168:171], v[18:21], v[42:45]
	v_mfma_f32_16x16x32_f16 v[118:121], v[168:171], v[34:37], v[50:53]
	v_mfma_f32_16x16x32_f16 v[42:45], v[146:149], v[6:9], 0
	v_mfma_f32_16x16x32_f16 v[50:53], v[146:149], v[22:25], 0
	v_mfma_f32_16x16x32_f16 v[42:45], v[154:157], v[10:13], v[42:45]
	v_mfma_f32_16x16x32_f16 v[50:53], v[154:157], v[26:29], v[50:53]
	v_mfma_f32_16x16x32_f16 v[42:45], v[162:165], v[14:17], v[42:45]
	v_mfma_f32_16x16x32_f16 v[50:53], v[162:165], v[30:33], v[50:53]
	v_mfma_f32_16x16x32_f16 v[42:45], v[194:197], v[18:21], v[42:45]
	v_mfma_f32_16x16x32_f16 v[50:53], v[194:197], v[34:37], v[50:53]
	v_max_f32_e32 v1, v131, v131
	v_max_f32_e32 v2, v130, v130
	v_max_f32_e32 v1, v2, v1
	v_max3_f32 v1, v1, v132, v133
	v_max3_f32 v1, v1, v38, v39
	v_max3_f32 v1, v1, v40, v41
	v_max3_f32 v1, v1, v126, v127
	v_max3_f32 v1, v1, v128, v129
	v_max3_f32 v1, v1, v42, v43
	v_max3_f32 v1, v1, v44, v45
	v_mul_f32_e32 v172, 0x3e0293ee, v1
	v_mov_b32_e32 v181, v136
	v_pk_add_f32 v[138:139], v[180:181], v[172:173]
	v_mov_b32_e32 v4, 1.0
	v_cmp_gt_f32_e32 vcc, v138, v139
	s_cbranch_vccz .LBB0_1233
	ds_bpermute_b32 v1, v245, v138
	v_max_f32_e32 v2, v138, v138
	v_mov_b32_e32 v139, v137
	s_waitcnt lgkmcnt(0)
	v_max_f32_e32 v1, v1, v1
	v_max_f32_e32 v1, v2, v1
	ds_bpermute_b32 v2, v246, v1
	s_waitcnt lgkmcnt(0)
	v_max3_f32 v138, v136, v1, v2
	v_sub_f32_e32 v1, v136, v138
	v_exp_f32_e32 v194, v1
	v_mov_b32_e32 v136, v138
	s_branch .LBB0_1234

.LBB0_1328:
	s_setprio 0
	s_cmp_lt_i32 s70, 6
	s_cselect_b64 s[2:3], -1, 0
	s_and_b64 s[0:1], s[2:3], s[0:1]
	s_andn2_b64 vcc, exec, s[0:1]
	s_cbranch_vccnz .LBB0_1417
	s_cmpk_gt_i32 s90, 0x3ff
	v_readfirstlane_b32 s8, v0
	s_cbranch_scc1 .LBB0_1355
	s_ashr_i32 s26, s90, 31
	s_lshr_b32 s2, s26, 29
	s_add_i32 s5, s90, s2
	s_and_b32 s2, s5, -8
	s_sub_i32 s6, s90, s2
	s_cmp_gt_i32 s6, -1
	s_cbranch_scc0 .LBB0_1332
	s_lshl_b32 s4, s6, 7
	s_cbranch_execz .LBB0_1333
	s_branch .LBB0_1334
